# k20: + staged counted vmcnt waits at first use in the GLU and out-projection epilogues (P6, P7)
# baseline (speedup 1.0000x reference)
;     __device__ __forceinline__ void operator()(EPI_ARGS) const {
;         const int j0 = u.pn * 128 + wc * 32 + 8 * fq, j0q = u.pn * 128 + wc * 32 + 8 * (fq & ~1);
;         f32x4 ba0, ba1, bb0, bb1; u32x4 glq[2][2], ypq[2][2][2];
;         EPI_ALD16(ba0, bglu + j0); EPI_ALD16(ba1, bglu + j0 + 4); EPI_ALD16(bb0, bglu + D + j0); EPI_ALD16(bb1, bglu + D + j0 + 4);
; #pragma unroll
;         for (int ai = 0; ai < 2; ++ai)
; #pragma unroll
;             for (int mp = 0; mp < 2; ++mp) {
;                 if (GATE_FP8) { const int rowq = u.pm * 256 + ai * 128 + wr * 64 + (2 * mp + (fq & 1)) * 16 + fr;
;                     const unsigned char* gp = (const unsigned char*)SGS + (size_t)rowq * D + j0q; EPI_ALD16(glq[ai][mp], gp); }
; #pragma unroll
;                 for (int h = 0; h < 2; ++h) { const int row = u.pm * 256 + ai * 128 + wr * 64 + (2 * mp + h) * 16 + fr; const bf16* yq = YPG + (size_t)row * D + j0; EPI_ALD16(ypq[ai][mp][h], yq); } }
;         asm volatile("s_waitcnt vmcnt(0)" : "+v"(ba0), "+v"(ba1), "+v"(bb0), "+v"(bb1), "+v"(ypq[0][0][0]), "+v"(ypq[0][0][1]), "+v"(ypq[0][1][0]), "+v"(ypq[0][1][1]), "+v"(ypq[1][0][0]), "+v"(ypq[1][0][1]), "+v"(ypq[1][1][0]), "+v"(ypq[1][1][1]));
;         if (GATE_FP8) asm volatile("" : "+v"(glq[0][0]), "+v"(glq[0][1]), "+v"(glq[1][0]), "+v"(glq[1][1]));
; #pragma unroll
;         for (int ai = 0; ai < 2; ++ai)
; #pragma unroll
;             for (int mp = 0; mp < 2; ++mp) { unsigned px[2], py[2]; unsigned gq[2][2] = {{0u, 0u}, {0u, 0u}};
;                 if (GATE_FP8) unpair16(glq[ai][mp], gq[0][0], gq[0][1], gq[1][0], gq[1][1]);
; #pragma unroll
;                 for (int h = 0; h < 2; ++h) { const int m = 2 * mp + h; const int row = u.pm * 256 + ai * 128 + wr * 64 + m * 16 + fr; const size_t off = (size_t)row * D + j0;
;                     const u32x4 yp = ypq[ai][mp][h]; float gsf[8];
;                     if (GATE_FP8) { v2u g8; g8.x = gq[h][0]; g8.y = gq[h][1]; const float k255 = 1.0f / 255.0f;
;                         gsf[0] = (float)(g8.x & 0xffu) * k255; gsf[1] = (float)((g8.x >> 8) & 0xffu) * k255; gsf[2] = (float)((g8.x >> 16) & 0xffu) * k255; gsf[3] = (float)(g8.x >> 24) * k255;
;                         gsf[4] = (float)(g8.y & 0xffu) * k255; gsf[5] = (float)((g8.y >> 8) & 0xffu) * k255; gsf[6] = (float)((g8.y >> 16) & 0xffu) * k255; gsf[7] = (float)(g8.y >> 24) * k255; }
.LBB0_906:
	s_lshl_b32 s14, s75, 7
	s_or_b32 s14, s14, s66
	v_or_b32_e32 v18, s14, v195
	v_or_b32_e32 v58, s14, v219
	s_lshl_b32 s14, s38, 8
	s_add_i32 s14, s14, s65
	v_or_b32_e32 v20, s14, v1
	v_ashrrev_i32_e32 v19, 31, v18
	v_or_b32_e32 v22, v20, v220
	v_lshlrev_b64 v[10:11], 2, v[18:19]
	v_ashrrev_i32_e32 v23, 31, v22
	v_lshl_add_u64 v[12:13], s[6:7], 0, v[10:11]
	v_lshlrev_b64 v[22:23], 11, v[22:23]
	v_lshl_add_u64 v[2:3], v[12:13], 0, 16
	v_lshl_add_u64 v[10:11], s[20:21], 0, v[10:11]
	v_ashrrev_i32_e32 v59, 31, v58
	v_lshl_add_u64 v[22:23], s[10:11], 0, v[22:23]
	s_nop 15
	s_nop 15
	global_load_dwordx4 v[6:9], v[12:13], off
	global_load_dwordx4 v[2:5], v[2:3], off
	global_load_dwordx4 v[14:17], v[10:11], off
	v_lshl_add_u64 v[10:11], v[12:13], 0, s[24:25]
	v_lshl_add_u64 v[22:23], v[22:23], 0, v[58:59]
	v_ashrrev_i32_e32 v21, 31, v20
	global_load_dwordx4 v[10:13], v[10:11], off
	global_load_dwordx4 v[62:65], v[22:23], off
	v_lshlrev_b64 v[22:23], 12, v[20:21]
	v_lshl_add_u64 v[22:23], s[12:13], 0, v[22:23]
	v_lshlrev_b64 v[18:19], 1, v[18:19]
	v_lshl_add_u64 v[22:23], v[22:23], 0, v[18:19]
	global_load_dwordx4 v[214:217], v[22:23], off
	v_or_b32_e32 v22, 16, v20
	v_ashrrev_i32_e32 v23, 31, v22
	v_lshlrev_b64 v[22:23], 12, v[22:23]
	v_lshl_add_u64 v[22:23], s[12:13], 0, v[22:23]
	v_lshl_add_u64 v[22:23], v[22:23], 0, v[18:19]
	global_load_dwordx4 v[54:57], v[22:23], off
	v_or_b32_e32 v22, v20, v221
	v_ashrrev_i32_e32 v23, 31, v22
	v_lshlrev_b64 v[22:23], 11, v[22:23]
	v_lshl_add_u64 v[22:23], s[10:11], 0, v[22:23]
	v_lshl_add_u64 v[22:23], v[22:23], 0, v[58:59]
	global_load_dwordx4 v[50:53], v[22:23], off
	v_or_b32_e32 v22, 32, v20
	v_or_b32_e32 v20, 48, v20
	v_ashrrev_i32_e32 v21, 31, v20
	v_ashrrev_i32_e32 v23, 31, v22
	v_lshlrev_b64 v[20:21], 12, v[20:21]
	v_lshlrev_b64 v[22:23], 12, v[22:23]
	v_lshl_add_u64 v[20:21], s[12:13], 0, v[20:21]
	v_lshl_add_u64 v[22:23], s[12:13], 0, v[22:23]
	v_lshl_add_u64 v[20:21], v[20:21], 0, v[18:19]
	v_lshl_add_u64 v[22:23], v[22:23], 0, v[18:19]
	global_load_dwordx4 v[46:49], v[22:23], off
	global_load_dwordx4 v[42:45], v[20:21], off
	v_add_u32_e32 v20, s14, v218
	v_or_b32_e32 v22, v20, v220
	v_ashrrev_i32_e32 v23, 31, v22
	v_lshlrev_b64 v[22:23], 11, v[22:23]
	v_lshl_add_u64 v[22:23], s[10:11], 0, v[22:23]
	v_lshl_add_u64 v[22:23], v[22:23], 0, v[58:59]
	v_ashrrev_i32_e32 v21, 31, v20
	global_load_dwordx4 v[38:41], v[22:23], off
	v_lshlrev_b64 v[22:23], 12, v[20:21]
	v_lshl_add_u64 v[22:23], s[12:13], 0, v[22:23]
	v_lshl_add_u64 v[22:23], v[22:23], 0, v[18:19]
	global_load_dwordx4 v[34:37], v[22:23], off
	v_or_b32_e32 v22, 16, v20
	v_ashrrev_i32_e32 v23, 31, v22
	v_lshlrev_b64 v[22:23], 12, v[22:23]
	v_lshl_add_u64 v[22:23], s[12:13], 0, v[22:23]
	v_lshl_add_u64 v[22:23], v[22:23], 0, v[18:19]
	global_load_dwordx4 v[30:33], v[22:23], off
	v_or_b32_e32 v22, v20, v221
	v_ashrrev_i32_e32 v23, 31, v22
	v_lshlrev_b64 v[22:23], 11, v[22:23]
	v_lshl_add_u64 v[22:23], s[10:11], 0, v[22:23]
	v_lshl_add_u64 v[22:23], v[22:23], 0, v[58:59]
	global_load_dwordx4 v[26:29], v[22:23], off
	v_or_b32_e32 v22, 32, v20
	v_or_b32_e32 v20, 48, v20
	v_ashrrev_i32_e32 v23, 31, v22
	v_ashrrev_i32_e32 v21, 31, v20
	v_lshlrev_b64 v[22:23], 12, v[22:23]
	v_lshlrev_b64 v[20:21], 12, v[20:21]
	v_lshl_add_u64 v[22:23], s[12:13], 0, v[22:23]
	v_lshl_add_u64 v[20:21], s[12:13], 0, v[20:21]
	v_lshl_add_u64 v[22:23], v[22:23], 0, v[18:19]
	v_lshl_add_u64 v[18:19], v[20:21], 0, v[18:19]
	global_load_dwordx4 v[22:25], v[22:23], off
	global_load_dwordx4 v[18:21], v[18:19], off
	v_or_b32_e32 v60, s14, v222
	s_andn2_b64 vcc, exec, s[4:5]
	s_waitcnt vmcnt(11)
	v_mov_b32_e32 v240, v65
	s_nop 1
	v_permlane16_swap_b32_e32 v63, v240
	v_cvt_f32_ubyte0_e32 v232, v63
	v_cvt_f32_ubyte1_e32 v234, v63
	v_cvt_f32_ubyte2_e32 v236, v63
	v_cvt_f32_ubyte3_e32 v238, v63
	v_fmamk_f32 v63, v182, 0x3d000000, v14
	v_mul_f32_e32 v63, 0xbfb8aa3b, v63
	v_fmamk_f32 v178, v178, 0x3d000000, v10
	v_exp_f32_e32 v63, v63
	v_mul_f32_e32 v178, 0xbfb8aa3b, v178
	v_exp_f32_e32 v178, v178
	v_fmamk_f32 v233, v186, 0x3d000000, v2
	v_add_f32_e32 v63, 1.0, v63
	v_rcp_f32_e32 v213, v63
	v_add_f32_e32 v63, 1.0, v178
	v_rcp_f32_e32 v182, v63
	v_fmamk_f32 v63, v183, 0x3d000000, v15
	v_mul_f32_e32 v63, 0xbfb8aa3b, v63
	v_fmamk_f32 v178, v179, 0x3d000000, v11
	v_exp_f32_e32 v63, v63
	v_mul_f32_e32 v178, 0xbfb8aa3b, v178
	v_exp_f32_e32 v178, v178
	v_fmamk_f32 v181, v181, 0x3d000000, v13
	v_add_f32_e32 v63, 1.0, v63
	v_rcp_f32_e32 v179, v63
	v_add_f32_e32 v63, 1.0, v178
	v_rcp_f32_e32 v186, v63
	v_fmamk_f32 v63, v184, 0x3d000000, v16
	v_mul_f32_e32 v63, 0xbfb8aa3b, v63
	v_fmamk_f32 v178, v180, 0x3d000000, v12
	v_exp_f32_e32 v63, v63
	v_mul_f32_e32 v178, 0xbfb8aa3b, v178
	v_exp_f32_e32 v178, v178
	v_mul_f32_e32 v181, 0xbfb8aa3b, v181
	v_add_f32_e32 v63, 1.0, v63
	v_rcp_f32_e32 v180, v63
	v_add_f32_e32 v63, 1.0, v178
	v_fmamk_f32 v178, v185, 0x3d000000, v17
	v_mul_f32_e32 v178, 0xbfb8aa3b, v178
	v_exp_f32_e32 v178, v178
	v_exp_f32_e32 v181, v181
	v_mov_b32_e32 v61, v64
	s_nop 1
	v_permlane16_swap_b32_e32 v62, v61
	v_add_f32_e32 v178, 1.0, v178
	v_rcp_f32_e32 v183, v178
	v_cvt_f32_ubyte0_e32 v64, v62
	v_fmamk_f32 v65, v190, 0x3d000000, v6
	v_cvt_f32_ubyte1_e32 v228, v62
	v_fmamk_f32 v229, v191, 0x3d000000, v7
	v_add_f32_e32 v178, 1.0, v181
	v_pk_mul_f32 v[64:65], v[64:65], v[212:213]
	v_mov_b32_e32 v213, v179
	v_cvt_f32_ubyte2_e32 v230, v62
	v_fmamk_f32 v231, v192, 0x3d000000, v8
	v_fmamk_f32 v237, v188, 0x3d000000, v4
	v_rcp_f32_e32 v188, v178
	v_pk_mul_f32 v[178:179], v[228:229], v[212:213]
	v_mov_b32_e32 v213, v180
	v_cvt_f32_ubyte3_e32 v62, v62
	v_fmamk_f32 v235, v187, 0x3d000000, v3
	v_rcp_f32_e32 v187, v63
	v_fmamk_f32 v63, v193, 0x3d000000, v9
	v_pk_mul_f32 v[180:181], v[230:231], v[212:213]
	v_mov_b32_e32 v213, v183
	s_waitcnt vmcnt(10)
;     __device__ __forceinline__ void operator()(EPI_ARGS) const {
;     ...
;             for (int mp = 0; mp < 2; ++mp) { unsigned px[2], py[2]; unsigned gq[2][2] = {{0u, 0u}, {0u, 0u}};
;                 if (GATE_FP8) unpair16(glq[ai][mp], gq[0][0], gq[0][1], gq[1][0], gq[1][1]);
; #pragma unroll
;                 for (int h = 0; h < 2; ++h) { const int m = 2 * mp + h; const int row = u.pm * 256 + ai * 128 + wr * 64 + m * 16 + fr; const size_t off = (size_t)row * D + j0;
;                     const u32x4 yp = ypq[ai][mp][h]; float gsf[8];
;                     if (GATE_FP8) { v2u g8; g8.x = gq[h][0]; g8.y = gq[h][1]; const float k255 = 1.0f / 255.0f;
;                         gsf[0] = (float)(g8.x & 0xffu) * k255; gsf[1] = (float)((g8.x >> 8) & 0xffu) * k255; gsf[2] = (float)((g8.x >> 16) & 0xffu) * k255; gsf[3] = (float)(g8.x >> 24) * k255;
;                         gsf[4] = (float)(g8.y & 0xffu) * k255; gsf[5] = (float)((g8.y >> 8) & 0xffu) * k255; gsf[6] = (float)((g8.y >> 16) & 0xffu) * k255; gsf[7] = (float)(g8.y >> 24) * k255; }
;                     else { const u32x4 gs = *(const u32x4*)(SGS + off); gsf[0] = bf_lo(gs.x); gsf[1] = bf_hi(gs.x); gsf[2] = bf_lo(gs.y); gsf[3] = bf_hi(gs.y); gsf[4] = bf_lo(gs.z); gsf[5] = bf_hi(gs.z); gsf[6] = bf_lo(gs.w); gsf[7] = bf_hi(gs.w); }
;                     const f32x4 a0 = acc[ai][0][m][0] * asc + ba0, a1 = acc[ai][0][m][1] * asc + ba1, b0 = acc[ai][1][m][0] * asc + bb0, b1 = acc[ai][1][m][1] * asc + bb1;
;                     float o[8];
; #pragma unroll
;                     for (int j = 0; j < 4; ++j) { o[j] = a0[j] * sigmoidf_(b0[j]); o[4 + j] = a1[j] * sigmoidf_(b1[j]); }
;                     float mo[8] = {bf_lo(yp.x) + gsf[0] * o[0], bf_hi(yp.x) + gsf[1] * o[1], bf_lo(yp.y) + gsf[2] * o[2], bf_hi(yp.y) + gsf[3] * o[3],
;                                    bf_lo(yp.z) + gsf[4] * o[4], bf_hi(yp.z) + gsf[5] * o[5], bf_lo(yp.w) + gsf[6] * o[6], bf_hi(yp.w) + gsf[7] * o[7]};
;                     if (OUT_FP8) { px[h] = pk4_fp8(mo[0], mo[1], mo[2], mo[3]); py[h] = pk4_fp8(mo[4], mo[5], mo[6], mo[7]); }
;                     else { u32x4 w; w.x = cvt_pk_bf16(mo[0], mo[1]); w.y = cvt_pk_bf16(mo[2], mo[3]); w.z = cvt_pk_bf16(mo[4], mo[5]); w.w = cvt_pk_bf16(mo[6], mo[7]); *(u32x4*)(MG + off) = w; } }
;                 if (OUT_FP8) { const u32x4 q = pair16(px[0], py[0], px[1], py[1]);
	v_lshlrev_b32_e32 v190, 16, v214
	v_pk_mul_f32 v[62:63], v[62:63], v[212:213]
	v_mov_b32_e32 v213, v182
	v_fmac_f32_e32 v190, v64, v65
	v_and_b32_e32 v64, 0xffff0000, v214
	v_pk_mul_f32 v[182:183], v[232:233], v[212:213]
	v_mov_b32_e32 v213, v186
	v_fmac_f32_e32 v64, v178, v179
	v_and_b32_e32 v178, 0xffff0000, v215
	v_pk_mul_f32 v[184:185], v[234:235], v[212:213]
	v_fmac_f32_e32 v178, v62, v63
	v_lshlrev_b32_e32 v63, 16, v216
	v_and_b32_e32 v179, 0xffff0000, v216
	v_fmac_f32_e32 v63, v182, v183
	v_fmac_f32_e32 v179, v184, v185
	v_med3_f32 v182, v190, s74, v227
	v_med3_f32 v64, v64, s74, v227
	v_mov_b32_e32 v62, 0
	v_fmamk_f32 v163, v163, 0x3d000000, v11
	v_mov_b32_e32 v213, v187
	v_cvt_pk_fp8_f32 v62, v182, v64
	v_med3_f32 v64, v63, s74, v227
	v_med3_f32 v179, v179, s74, v227
	v_mov_b32_e32 v63, 0
	v_mul_f32_e32 v163, 0xbfb8aa3b, v163
	v_fmamk_f32 v239, v189, 0x3d000000, v5
	v_pk_mul_f32 v[186:187], v[236:237], v[212:213]
	v_mov_b32_e32 v213, v188
	v_lshlrev_b32_e32 v65, 16, v215
	v_cvt_pk_fp8_f32 v63, v64, v179
	v_exp_f32_e32 v163, v163
	v_pk_mul_f32 v[188:189], v[238:239], v[212:213]
	v_fmac_f32_e32 v65, v180, v181
	v_lshlrev_b32_e32 v180, 16, v217
	v_and_b32_e32 v181, 0xffff0000, v217
	v_fmac_f32_e32 v180, v186, v187
	v_fmac_f32_e32 v181, v188, v189
	v_med3_f32 v65, v65, s74, v227
	v_med3_f32 v178, v178, s74, v227
	v_cvt_pk_fp8_f32 v62, v65, v178 op_sel:[0,0,1]
	v_med3_f32 v64, v180, s74, v227
	v_med3_f32 v65, v181, s74, v227
	v_cvt_pk_fp8_f32 v63, v64, v65 op_sel:[0,0,1]
	v_cvt_f32_ubyte0_e32 v64, v61
	v_cvt_f32_ubyte1_e32 v178, v61
	v_cvt_f32_ubyte2_e32 v180, v61
	v_cvt_f32_ubyte3_e32 v182, v61
	v_fmamk_f32 v61, v166, 0x3d000000, v14
	v_add_f32_e32 v163, 1.0, v163
	v_mul_f32_e32 v61, 0xbfb8aa3b, v61
	v_fmamk_f32 v162, v162, 0x3d000000, v10
	v_fmamk_f32 v185, v170, 0x3d000000, v2
	v_rcp_f32_e32 v170, v163
	v_fmamk_f32 v163, v168, 0x3d000000, v16
	v_exp_f32_e32 v61, v61
	v_mul_f32_e32 v162, 0xbfb8aa3b, v162
	v_mul_f32_e32 v163, 0xbfb8aa3b, v163
	v_fmamk_f32 v164, v164, 0x3d000000, v12
	v_exp_f32_e32 v162, v162
	v_exp_f32_e32 v163, v163
	v_mul_f32_e32 v164, 0xbfb8aa3b, v164
	v_exp_f32_e32 v164, v164
	v_add_f32_e32 v61, 1.0, v61
	v_rcp_f32_e32 v213, v61
	v_add_f32_e32 v61, 1.0, v162
	v_fmamk_f32 v162, v167, 0x3d000000, v15
	v_add_f32_e32 v163, 1.0, v163
	v_mul_f32_e32 v162, 0xbfb8aa3b, v162
	v_rcp_f32_e32 v166, v163
	v_add_f32_e32 v163, 1.0, v164
	v_exp_f32_e32 v162, v162
	v_fmamk_f32 v189, v172, 0x3d000000, v4
	v_rcp_f32_e32 v172, v163
	v_fmamk_f32 v163, v169, 0x3d000000, v17
	v_mul_f32_e32 v163, 0xbfb8aa3b, v163
	v_exp_f32_e32 v163, v163
	v_fmamk_f32 v164, v165, 0x3d000000, v13
	v_add_f32_e32 v162, 1.0, v162
	v_mul_f32_e32 v164, 0xbfb8aa3b, v164
	v_rcp_f32_e32 v162, v162
	v_exp_f32_e32 v164, v164
	v_add_f32_e32 v163, 1.0, v163
	v_rcp_f32_e32 v167, v163
	v_fmamk_f32 v65, v174, 0x3d000000, v6
	v_rcp_f32_e32 v61, v61
	v_fmamk_f32 v179, v175, 0x3d000000, v7
	v_add_f32_e32 v163, 1.0, v164
	v_pk_mul_f32 v[64:65], v[64:65], v[212:213]
	v_mov_b32_e32 v213, v162
	v_fmamk_f32 v181, v176, 0x3d000000, v8
	v_rcp_f32_e32 v174, v163
	v_pk_mul_f32 v[162:163], v[178:179], v[212:213]
	v_mov_b32_e32 v213, v166
	v_fmamk_f32 v183, v177, 0x3d000000, v9
	v_pk_mul_f32 v[164:165], v[180:181], v[212:213]
	v_mov_b32_e32 v213, v167
	v_cvt_f32_ubyte0_e32 v184, v240
	v_pk_mul_f32 v[166:167], v[182:183], v[212:213]
	v_mov_b32_e32 v213, v61
	s_waitcnt vmcnt(9)
	v_lshlrev_b32_e32 v61, 16, v54
	v_cvt_f32_ubyte1_e32 v186, v240
	v_fmamk_f32 v187, v171, 0x3d000000, v3
	v_pk_mul_f32 v[168:169], v[184:185], v[212:213]
	v_mov_b32_e32 v213, v170
	v_fmac_f32_e32 v61, v64, v65
	v_and_b32_e32 v54, 0xffff0000, v54
	v_lshlrev_b32_e32 v64, 16, v55
	v_pk_mul_f32 v[170:171], v[186:187], v[212:213]
	v_fmac_f32_e32 v54, v162, v163
	v_fmac_f32_e32 v64, v164, v165
	v_lshlrev_b32_e32 v65, 16, v56
	v_and_b32_e32 v56, 0xffff0000, v56
	v_fmac_f32_e32 v65, v168, v169
	v_fmac_f32_e32 v56, v170, v171
	v_med3_f32 v61, v61, s74, v227
	v_med3_f32 v54, v54, s74, v227
	v_med3_f32 v163, v64, s74, v227
	v_mov_b32_e32 v64, 0
	v_cvt_f32_ubyte2_e32 v188, v240
	v_mov_b32_e32 v213, v172
	v_cvt_pk_fp8_f32 v64, v61, v54
	v_med3_f32 v54, v65, s74, v227
	v_med3_f32 v56, v56, s74, v227
	v_mov_b32_e32 v65, 0
	v_cvt_f32_ubyte3_e32 v190, v240
	v_fmamk_f32 v191, v173, 0x3d000000, v5
	v_pk_mul_f32 v[172:173], v[188:189], v[212:213]
	v_mov_b32_e32 v213, v174
	v_and_b32_e32 v55, 0xffff0000, v55
	v_cvt_pk_fp8_f32 v65, v54, v56
	v_pk_mul_f32 v[174:175], v[190:191], v[212:213]
	v_fmac_f32_e32 v55, v166, v167
	v_lshlrev_b32_e32 v162, 16, v57
	v_and_b32_e32 v57, 0xffff0000, v57
	v_fmac_f32_e32 v162, v172, v173
	v_fmac_f32_e32 v57, v174, v175
	v_med3_f32 v55, v55, s74, v227
	v_cvt_pk_fp8_f32 v64, v163, v55 op_sel:[0,0,1]
	v_med3_f32 v54, v162, s74, v227
	v_med3_f32 v55, v57, s74, v227
	v_cvt_pk_fp8_f32 v65, v54, v55 op_sel:[0,0,1]
	v_ashrrev_i32_e32 v61, 31, v60
	v_lshlrev_b64 v[54:55], 11, v[60:61]
	v_lshl_add_u64 v[54:55], s[16:17], 0, v[54:55]
	s_waitcnt vmcnt(8)
;     __device__ __forceinline__ void operator()(EPI_ARGS) const {
;     ...
;             for (int mp = 0; mp < 2; ++mp) { unsigned px[2], py[2]; unsigned gq[2][2] = {{0u, 0u}, {0u, 0u}};
;                 if (GATE_FP8) unpair16(glq[ai][mp], gq[0][0], gq[0][1], gq[1][0], gq[1][1]);
; #pragma unroll
;                 for (int h = 0; h < 2; ++h) { const int m = 2 * mp + h; const int row = u.pm * 256 + ai * 128 + wr * 64 + m * 16 + fr; const size_t off = (size_t)row * D + j0;
;                     const u32x4 yp = ypq[ai][mp][h]; float gsf[8];
;                     if (GATE_FP8) { v2u g8; g8.x = gq[h][0]; g8.y = gq[h][1]; const float k255 = 1.0f / 255.0f;
;                         gsf[0] = (float)(g8.x & 0xffu) * k255; gsf[1] = (float)((g8.x >> 8) & 0xffu) * k255; gsf[2] = (float)((g8.x >> 16) & 0xffu) * k255; gsf[3] = (float)(g8.x >> 24) * k255;
;                         gsf[4] = (float)(g8.y & 0xffu) * k255; gsf[5] = (float)((g8.y >> 8) & 0xffu) * k255; gsf[6] = (float)((g8.y >> 16) & 0xffu) * k255; gsf[7] = (float)(g8.y >> 24) * k255; }
;                     else { const u32x4 gs = *(const u32x4*)(SGS + off); gsf[0] = bf_lo(gs.x); gsf[1] = bf_hi(gs.x); gsf[2] = bf_lo(gs.y); gsf[3] = bf_hi(gs.y); gsf[4] = bf_lo(gs.z); gsf[5] = bf_hi(gs.z); gsf[6] = bf_lo(gs.w); gsf[7] = bf_hi(gs.w); }
;                     const f32x4 a0 = acc[ai][0][m][0] * asc + ba0, a1 = acc[ai][0][m][1] * asc + ba1, b0 = acc[ai][1][m][0] * asc + bb0, b1 = acc[ai][1][m][1] * asc + bb1;
;                     float o[8];
; #pragma unroll
;                     for (int j = 0; j < 4; ++j) { o[j] = a0[j] * sigmoidf_(b0[j]); o[4 + j] = a1[j] * sigmoidf_(b1[j]); }
;                     float mo[8] = {bf_lo(yp.x) + gsf[0] * o[0], bf_hi(yp.x) + gsf[1] * o[1], bf_lo(yp.y) + gsf[2] * o[2], bf_hi(yp.y) + gsf[3] * o[3],
;                                    bf_lo(yp.z) + gsf[4] * o[4], bf_hi(yp.z) + gsf[5] * o[5], bf_lo(yp.w) + gsf[6] * o[6], bf_hi(yp.w) + gsf[7] * o[7]};
;                     if (OUT_FP8) { px[h] = pk4_fp8(mo[0], mo[1], mo[2], mo[3]); py[h] = pk4_fp8(mo[4], mo[5], mo[6], mo[7]); }
;                     else { u32x4 w; w.x = cvt_pk_bf16(mo[0], mo[1]); w.y = cvt_pk_bf16(mo[2], mo[3]); w.z = cvt_pk_bf16(mo[4], mo[5]); w.w = cvt_pk_bf16(mo[6], mo[7]); *(u32x4*)(MG + off) = w; } }
;                 if (OUT_FP8) { const u32x4 q = pair16(px[0], py[0], px[1], py[1]);
	v_mov_b32_e32 v61, v52
	v_permlane16_swap_b32_e32 v62, v64
	v_permlane16_swap_b32_e32 v63, v65
	v_lshl_add_u64 v[54:55], v[54:55], 0, v[58:59]
	v_permlane16_swap_b32_e32 v50, v61
	global_store_dwordx4 v[54:55], v[62:65], off
	v_mov_b32_e32 v166, v53
	v_cvt_f32_ubyte0_e32 v53, v50
	v_cvt_f32_ubyte1_e32 v55, v50
	v_cvt_f32_ubyte2_e32 v57, v50
	v_cvt_f32_ubyte3_e32 v63, v50
	v_fmamk_f32 v50, v150, 0x3d000000, v14
	v_mul_f32_e32 v50, 0xbfb8aa3b, v50
	v_fmamk_f32 v54, v146, 0x3d000000, v10
	v_exp_f32_e32 v50, v50
	v_mul_f32_e32 v54, 0xbfb8aa3b, v54
	v_exp_f32_e32 v54, v54
	v_fmamk_f32 v56, v147, 0x3d000000, v11
	v_add_f32_e32 v50, 1.0, v50
	v_rcp_f32_e32 v146, v50
	v_add_f32_e32 v50, 1.0, v54
	v_rcp_f32_e32 v150, v50
	v_fmamk_f32 v50, v151, 0x3d000000, v15
	v_mul_f32_e32 v50, 0xbfb8aa3b, v50
	v_exp_f32_e32 v50, v50
	v_mul_f32_e32 v56, 0xbfb8aa3b, v56
	v_exp_f32_e32 v56, v56
	v_fmamk_f32 v64, v154, 0x3d000000, v2
	v_add_f32_e32 v50, 1.0, v50
	v_rcp_f32_e32 v154, v50
	v_add_f32_e32 v50, 1.0, v56
	v_fmamk_f32 v52, v158, 0x3d000000, v6
	v_rcp_f32_e32 v158, v50
	v_fmamk_f32 v50, v152, 0x3d000000, v16
	v_mul_f32_e32 v50, 0xbfb8aa3b, v50
	v_fmamk_f32 v62, v148, 0x3d000000, v12
	v_exp_f32_e32 v50, v50
	v_mul_f32_e32 v62, 0xbfb8aa3b, v62
	v_exp_f32_e32 v62, v62
	v_fmamk_f32 v147, v149, 0x3d000000, v13
	v_add_f32_e32 v50, 1.0, v50
	v_rcp_f32_e32 v148, v50
	v_add_f32_e32 v50, 1.0, v62
	v_mul_f32_e32 v147, 0xbfb8aa3b, v147
	v_rcp_f32_e32 v152, v50
	v_fmamk_f32 v50, v153, 0x3d000000, v17
	v_exp_f32_e32 v147, v147
	v_mul_f32_e32 v50, 0xbfb8aa3b, v50
	v_exp_f32_e32 v50, v50
	v_fmamk_f32 v56, v160, 0x3d000000, v8
	v_add_f32_e32 v147, 1.0, v147
	v_rcp_f32_e32 v160, v147
	v_permlane16_swap_b32_e32 v51, v166
	v_add_f32_e32 v50, 1.0, v50
	v_cvt_f32_ubyte0_e32 v65, v51
	v_fmamk_f32 v54, v159, 0x3d000000, v7
	v_fmamk_f32 v162, v155, 0x3d000000, v3
	v_fmamk_f32 v164, v156, 0x3d000000, v4
	v_rcp_f32_e32 v156, v50
	v_mov_b32_e32 v147, v212
	v_mov_b32_e32 v155, v212
	v_mov_b32_e32 v151, v212
	v_cvt_f32_ubyte1_e32 v163, v51
	v_cvt_f32_ubyte2_e32 v165, v51
	v_cvt_f32_ubyte3_e32 v51, v51
	v_fmamk_f32 v62, v161, 0x3d000000, v9
	v_fmamk_f32 v50, v157, 0x3d000000, v5
	v_pk_mul_f32 v[52:53], v[52:53], v[146:147]
	v_pk_mul_f32 v[54:55], v[54:55], v[154:155]
	v_pk_mul_f32 v[64:65], v[64:65], v[150:151]
	v_mov_b32_e32 v161, v212
	s_waitcnt vmcnt(8)
	v_lshlrev_b32_e32 v150, 16, v46
	v_and_b32_e32 v46, 0xffff0000, v46
	v_pk_mul_f32 v[50:51], v[50:51], v[160:161]
	v_fmac_f32_e32 v150, v52, v53
	v_fmac_f32_e32 v46, v54, v55
	v_lshlrev_b32_e32 v54, 16, v49
	v_and_b32_e32 v49, 0xffff0000, v49
	v_mov_b32_e32 v157, v212
	v_mov_b32_e32 v159, v212
	v_fmac_f32_e32 v49, v50, v51
	v_med3_f32 v50, v150, s74, v227
	v_med3_f32 v51, v46, s74, v227
	v_mov_b32_e32 v46, 0
	v_mov_b32_e32 v149, v212
	v_pk_mul_f32 v[62:63], v[62:63], v[156:157]
	v_pk_mul_f32 v[146:147], v[162:163], v[158:159]
	v_lshlrev_b32_e32 v52, 16, v47
	v_and_b32_e32 v47, 0xffff0000, v47
	v_lshlrev_b32_e32 v53, 16, v48
	v_and_b32_e32 v48, 0xffff0000, v48
	v_cvt_pk_fp8_f32 v46, v50, v51
	v_pk_mul_f32 v[56:57], v[56:57], v[148:149]
	v_fmac_f32_e32 v47, v62, v63
	v_fmac_f32_e32 v53, v64, v65
	v_fmac_f32_e32 v48, v146, v147
	v_fmac_f32_e32 v52, v56, v57
	v_med3_f32 v55, v47, s74, v227
	v_med3_f32 v50, v53, s74, v227
	v_med3_f32 v48, v48, s74, v227
	v_mov_b32_e32 v47, 0
	v_med3_f32 v52, v52, s74, v227
	v_cvt_pk_fp8_f32 v47, v50, v48
	v_fmamk_f32 v50, v134, 0x3d000000, v14
	v_cvt_pk_fp8_f32 v46, v52, v55 op_sel:[0,0,1]
	v_mul_f32_e32 v50, 0xbfb8aa3b, v50
	v_fmamk_f32 v52, v130, 0x3d000000, v10
	v_exp_f32_e32 v50, v50
	v_mul_f32_e32 v52, 0xbfb8aa3b, v52
	v_exp_f32_e32 v52, v52
	v_mov_b32_e32 v153, v212
	v_pk_mul_f32 v[148:149], v[164:165], v[152:153]
	v_add_f32_e32 v50, 1.0, v50
	v_fmac_f32_e32 v54, v148, v149
	v_rcp_f32_e32 v130, v50
	v_add_f32_e32 v50, 1.0, v52
	v_fmamk_f32 v52, v135, 0x3d000000, v15
	v_med3_f32 v48, v54, s74, v227
	v_mul_f32_e32 v52, 0xbfb8aa3b, v52
	v_fmamk_f32 v54, v131, 0x3d000000, v11
	v_exp_f32_e32 v52, v52
	v_mul_f32_e32 v54, 0xbfb8aa3b, v54
	v_exp_f32_e32 v54, v54
	v_med3_f32 v49, v49, s74, v227
	v_add_f32_e32 v52, 1.0, v52
	v_fmamk_f32 v56, v138, 0x3d000000, v2
	v_rcp_f32_e32 v138, v52
	v_add_f32_e32 v52, 1.0, v54
	v_fmamk_f32 v54, v136, 0x3d000000, v16
	v_cvt_pk_fp8_f32 v47, v48, v49 op_sel:[0,0,1]
	v_cvt_f32_ubyte0_e32 v49, v61
	v_cvt_f32_ubyte1_e32 v51, v61
	v_cvt_f32_ubyte2_e32 v53, v61
	v_cvt_f32_ubyte3_e32 v55, v61
	v_mul_f32_e32 v54, 0xbfb8aa3b, v54
	v_fmamk_f32 v61, v132, 0x3d000000, v12
	v_exp_f32_e32 v54, v54
	v_mul_f32_e32 v61, 0xbfb8aa3b, v61
	v_exp_f32_e32 v61, v61
	v_fmamk_f32 v131, v133, 0x3d000000, v13
	v_add_f32_e32 v54, 1.0, v54
	v_rcp_f32_e32 v132, v54
	v_add_f32_e32 v54, 1.0, v61
	v_fmamk_f32 v61, v137, 0x3d000000, v17
	v_mul_f32_e32 v61, 0xbfb8aa3b, v61
	v_exp_f32_e32 v61, v61
	v_mul_f32_e32 v131, 0xbfb8aa3b, v131
	v_exp_f32_e32 v131, v131
	v_fmamk_f32 v48, v142, 0x3d000000, v6
	v_rcp_f32_e32 v134, v50
	v_rcp_f32_e32 v142, v52
	v_add_f32_e32 v61, 1.0, v61
	v_fmamk_f32 v64, v140, 0x3d000000, v4
	v_rcp_f32_e32 v140, v61
	v_add_f32_e32 v61, 1.0, v131
	v_mov_b32_e32 v131, v212
	v_fmamk_f32 v50, v143, 0x3d000000, v7
	v_fmamk_f32 v62, v139, 0x3d000000, v3
	v_fmamk_f32 v52, v144, 0x3d000000, v8
	v_rcp_f32_e32 v144, v61
	v_pk_mul_f32 v[48:49], v[48:49], v[130:131]
	v_mov_b32_e32 v139, v212
	v_mov_b32_e32 v133, v212
	s_waitcnt vmcnt(7)
;     __device__ __forceinline__ void operator()(EPI_ARGS) const {
;     ...
;             for (int mp = 0; mp < 2; ++mp) { unsigned px[2], py[2]; unsigned gq[2][2] = {{0u, 0u}, {0u, 0u}};
;                 if (GATE_FP8) unpair16(glq[ai][mp], gq[0][0], gq[0][1], gq[1][0], gq[1][1]);
; #pragma unroll
;                 for (int h = 0; h < 2; ++h) { const int m = 2 * mp + h; const int row = u.pm * 256 + ai * 128 + wr * 64 + m * 16 + fr; const size_t off = (size_t)row * D + j0;
;                     const u32x4 yp = ypq[ai][mp][h]; float gsf[8];
;                     if (GATE_FP8) { v2u g8; g8.x = gq[h][0]; g8.y = gq[h][1]; const float k255 = 1.0f / 255.0f;
;                         gsf[0] = (float)(g8.x & 0xffu) * k255; gsf[1] = (float)((g8.x >> 8) & 0xffu) * k255; gsf[2] = (float)((g8.x >> 16) & 0xffu) * k255; gsf[3] = (float)(g8.x >> 24) * k255;
;                         gsf[4] = (float)(g8.y & 0xffu) * k255; gsf[5] = (float)((g8.y >> 8) & 0xffu) * k255; gsf[6] = (float)((g8.y >> 16) & 0xffu) * k255; gsf[7] = (float)(g8.y >> 24) * k255; }
;                     else { const u32x4 gs = *(const u32x4*)(SGS + off); gsf[0] = bf_lo(gs.x); gsf[1] = bf_hi(gs.x); gsf[2] = bf_lo(gs.y); gsf[3] = bf_hi(gs.y); gsf[4] = bf_lo(gs.z); gsf[5] = bf_hi(gs.z); gsf[6] = bf_lo(gs.w); gsf[7] = bf_hi(gs.w); }
;                     const f32x4 a0 = acc[ai][0][m][0] * asc + ba0, a1 = acc[ai][0][m][1] * asc + ba1, b0 = acc[ai][1][m][0] * asc + bb0, b1 = acc[ai][1][m][1] * asc + bb1;
;                     float o[8];
; #pragma unroll
;                     for (int j = 0; j < 4; ++j) { o[j] = a0[j] * sigmoidf_(b0[j]); o[4 + j] = a1[j] * sigmoidf_(b1[j]); }
;                     float mo[8] = {bf_lo(yp.x) + gsf[0] * o[0], bf_hi(yp.x) + gsf[1] * o[1], bf_lo(yp.y) + gsf[2] * o[2], bf_hi(yp.y) + gsf[3] * o[3],
;                                    bf_lo(yp.z) + gsf[4] * o[4], bf_hi(yp.z) + gsf[5] * o[5], bf_lo(yp.w) + gsf[6] * o[6], bf_hi(yp.w) + gsf[7] * o[7]};
;                     if (OUT_FP8) { px[h] = pk4_fp8(mo[0], mo[1], mo[2], mo[3]); py[h] = pk4_fp8(mo[4], mo[5], mo[6], mo[7]); }
;                     else { u32x4 w; w.x = cvt_pk_bf16(mo[0], mo[1]); w.y = cvt_pk_bf16(mo[2], mo[3]); w.z = cvt_pk_bf16(mo[4], mo[5]); w.w = cvt_pk_bf16(mo[6], mo[7]); *(u32x4*)(MG + off) = w; } }
;                 if (OUT_FP8) { const u32x4 q = pair16(px[0], py[0], px[1], py[1]);
	v_lshlrev_b32_e32 v61, 16, v42
	v_cvt_f32_ubyte0_e32 v57, v166
	v_cvt_f32_ubyte1_e32 v63, v166
	v_pk_mul_f32 v[50:51], v[50:51], v[138:139]
	v_pk_mul_f32 v[52:53], v[52:53], v[132:133]
	v_mov_b32_e32 v135, v212
	v_mov_b32_e32 v143, v212
	v_fmac_f32_e32 v61, v48, v49
	v_and_b32_e32 v42, 0xffff0000, v42
	v_lshlrev_b32_e32 v48, 16, v43
	v_rcp_f32_e32 v136, v54
	v_pk_mul_f32 v[56:57], v[56:57], v[134:135]
	v_pk_mul_f32 v[62:63], v[62:63], v[142:143]
	v_fmac_f32_e32 v42, v50, v51
	v_fmac_f32_e32 v48, v52, v53
	v_lshlrev_b32_e32 v49, 16, v44
	v_and_b32_e32 v44, 0xffff0000, v44
	v_fmac_f32_e32 v49, v56, v57
	v_fmac_f32_e32 v44, v62, v63
	v_med3_f32 v51, v61, s74, v227
	v_med3_f32 v42, v42, s74, v227
	v_med3_f32 v52, v48, s74, v227
	v_mov_b32_e32 v48, 0
	v_fmamk_f32 v54, v145, 0x3d000000, v9
	v_fmamk_f32 v146, v141, 0x3d000000, v5
	v_mov_b32_e32 v141, v212
	v_cvt_pk_fp8_f32 v48, v51, v42
	v_med3_f32 v42, v49, s74, v227
	v_med3_f32 v44, v44, s74, v227
	v_mov_b32_e32 v49, 0
	v_cvt_f32_ubyte2_e32 v65, v166
	v_cvt_f32_ubyte3_e32 v147, v166
	v_pk_mul_f32 v[54:55], v[54:55], v[140:141]
	v_mov_b32_e32 v137, v212
	v_mov_b32_e32 v145, v212
	v_and_b32_e32 v43, 0xffff0000, v43
	v_cvt_pk_fp8_f32 v49, v42, v44
	v_pk_mul_f32 v[64:65], v[64:65], v[136:137]
	v_pk_mul_f32 v[130:131], v[146:147], v[144:145]
	v_fmac_f32_e32 v43, v54, v55
	v_lshlrev_b32_e32 v50, 16, v45
	v_and_b32_e32 v45, 0xffff0000, v45
	v_fmac_f32_e32 v50, v64, v65
	v_fmac_f32_e32 v45, v130, v131
	v_med3_f32 v43, v43, s74, v227
	v_cvt_pk_fp8_f32 v48, v52, v43 op_sel:[0,0,1]
	v_med3_f32 v42, v50, s74, v227
	v_med3_f32 v43, v45, s74, v227
	v_cvt_pk_fp8_f32 v49, v42, v43 op_sel:[0,0,1]
	v_or_b32_e32 v42, 32, v60
	v_ashrrev_i32_e32 v43, 31, v42
	v_lshlrev_b64 v[42:43], 11, v[42:43]
	v_lshl_add_u64 v[42:43], s[16:17], 0, v[42:43]
	v_permlane16_swap_b32_e32 v46, v48
	v_permlane16_swap_b32_e32 v47, v49
	v_lshl_add_u64 v[42:43], v[42:43], 0, v[58:59]
	global_store_dwordx4 v[42:43], v[46:49], off
	s_waitcnt vmcnt(7)
	v_mov_b32_e32 v43, v40
	s_nop 1
	v_permlane16_swap_b32_e32 v38, v43
	v_mov_b32_e32 v61, v41
	v_cvt_f32_ubyte0_e32 v41, v38
	v_cvt_f32_ubyte1_e32 v45, v38
	v_cvt_f32_ubyte2_e32 v47, v38
	v_cvt_f32_ubyte3_e32 v49, v38
	v_fmamk_f32 v38, v126, 0x3d000000, v14
	v_mul_f32_e32 v38, 0xbfb8aa3b, v38
	v_fmamk_f32 v44, v122, 0x3d000000, v10
	v_exp_f32_e32 v38, v38
	v_mul_f32_e32 v44, 0xbfb8aa3b, v44
	v_exp_f32_e32 v44, v44
	v_fmamk_f32 v46, v123, 0x3d000000, v11
	v_add_f32_e32 v38, 1.0, v38
	v_rcp_f32_e32 v56, v38
	v_add_f32_e32 v38, 1.0, v44
	v_rcp_f32_e32 v62, v38
	v_fmamk_f32 v38, v127, 0x3d000000, v15
	v_mul_f32_e32 v38, 0xbfb8aa3b, v38
	v_exp_f32_e32 v38, v38
	v_mul_f32_e32 v46, 0xbfb8aa3b, v46
	v_exp_f32_e32 v46, v46
	v_fmamk_f32 v50, v114, 0x3d000000, v2
	v_add_f32_e32 v38, 1.0, v38
	v_rcp_f32_e32 v64, v38
	v_add_f32_e32 v38, 1.0, v46
	v_rcp_f32_e32 v114, v38
	v_fmamk_f32 v38, v128, 0x3d000000, v16
	v_mul_f32_e32 v38, 0xbfb8aa3b, v38
	v_fmamk_f32 v48, v124, 0x3d000000, v12
	v_exp_f32_e32 v38, v38
	v_mul_f32_e32 v48, 0xbfb8aa3b, v48
	v_exp_f32_e32 v48, v48
	v_fmamk_f32 v57, v125, 0x3d000000, v13
	v_add_f32_e32 v38, 1.0, v38
	v_fmamk_f32 v40, v118, 0x3d000000, v6
	v_rcp_f32_e32 v118, v38
	v_add_f32_e32 v38, 1.0, v48
	v_mul_f32_e32 v57, 0xbfb8aa3b, v57
	v_fmamk_f32 v54, v116, 0x3d000000, v4
	v_rcp_f32_e32 v116, v38
	v_fmamk_f32 v38, v129, 0x3d000000, v17
	v_exp_f32_e32 v57, v57
	v_mul_f32_e32 v38, 0xbfb8aa3b, v38
	v_exp_f32_e32 v38, v38
	v_permlane16_swap_b32_e32 v39, v61
	v_add_f32_e32 v57, 1.0, v57
	v_rcp_f32_e32 v122, v57
	v_add_f32_e32 v38, 1.0, v38
	v_fmamk_f32 v44, v119, 0x3d000000, v7
	v_fmamk_f32 v46, v120, 0x3d000000, v8
	v_rcp_f32_e32 v120, v38
	v_mov_b32_e32 v57, v212
	v_mov_b32_e32 v65, v212
	v_cvt_f32_ubyte0_e32 v51, v39
	v_cvt_f32_ubyte1_e32 v53, v39
	v_cvt_f32_ubyte2_e32 v55, v39
	v_cvt_f32_ubyte3_e32 v39, v39
	v_fmamk_f32 v38, v117, 0x3d000000, v5
	v_pk_mul_f32 v[40:41], v[40:41], v[56:57]
	v_pk_mul_f32 v[44:45], v[44:45], v[64:65]
	v_mov_b32_e32 v123, v212
	s_waitcnt vmcnt(6)
	v_lshlrev_b32_e32 v56, 16, v34
	v_and_b32_e32 v34, 0xffff0000, v34
	v_pk_mul_f32 v[38:39], v[38:39], v[122:123]
	v_fmac_f32_e32 v56, v40, v41
	v_fmac_f32_e32 v34, v44, v45
	v_lshlrev_b32_e32 v44, 16, v37
	v_and_b32_e32 v37, 0xffff0000, v37
	v_fmamk_f32 v52, v115, 0x3d000000, v3
	v_fmamk_f32 v48, v121, 0x3d000000, v9
	v_mov_b32_e32 v121, v212
	v_mov_b32_e32 v63, v212
	v_mov_b32_e32 v115, v212
	v_fmac_f32_e32 v37, v38, v39
	v_med3_f32 v38, v56, s74, v227
	v_med3_f32 v39, v34, s74, v227
	v_mov_b32_e32 v34, 0
	v_mov_b32_e32 v119, v212
	v_pk_mul_f32 v[48:49], v[48:49], v[120:121]
	v_pk_mul_f32 v[50:51], v[50:51], v[62:63]
	v_pk_mul_f32 v[52:53], v[52:53], v[114:115]
	v_lshlrev_b32_e32 v40, 16, v35
	v_and_b32_e32 v35, 0xffff0000, v35
	v_lshlrev_b32_e32 v41, 16, v36
	v_and_b32_e32 v36, 0xffff0000, v36
	v_cvt_pk_fp8_f32 v34, v38, v39
	v_pk_mul_f32 v[46:47], v[46:47], v[118:119]
	v_fmac_f32_e32 v35, v48, v49
	v_fmac_f32_e32 v41, v50, v51
	v_fmac_f32_e32 v36, v52, v53
	v_fmac_f32_e32 v40, v46, v47
	v_med3_f32 v45, v35, s74, v227
	v_med3_f32 v38, v41, s74, v227
	v_med3_f32 v36, v36, s74, v227
	v_mov_b32_e32 v35, 0
	v_med3_f32 v40, v40, s74, v227
	v_cvt_pk_fp8_f32 v35, v38, v36
	v_fmamk_f32 v38, v110, 0x3d000000, v14
	v_cvt_pk_fp8_f32 v34, v40, v45 op_sel:[0,0,1]
	v_mul_f32_e32 v38, 0xbfb8aa3b, v38
	v_fmamk_f32 v40, v106, 0x3d000000, v10
	v_exp_f32_e32 v38, v38
	v_mul_f32_e32 v40, 0xbfb8aa3b, v40
	v_exp_f32_e32 v40, v40
	v_mov_b32_e32 v117, v212
	v_pk_mul_f32 v[54:55], v[54:55], v[116:117]
	v_add_f32_e32 v38, 1.0, v38
	v_fmac_f32_e32 v44, v54, v55
	v_med3_f32 v36, v44, s74, v227
	v_med3_f32 v37, v37, s74, v227
;     __device__ __forceinline__ void operator()(EPI_ARGS) const {
;     ...
;             for (int mp = 0; mp < 2; ++mp) { unsigned px[2], py[2]; unsigned gq[2][2] = {{0u, 0u}, {0u, 0u}};
;                 if (GATE_FP8) unpair16(glq[ai][mp], gq[0][0], gq[0][1], gq[1][0], gq[1][1]);
; #pragma unroll
;                 for (int h = 0; h < 2; ++h) { const int m = 2 * mp + h; const int row = u.pm * 256 + ai * 128 + wr * 64 + m * 16 + fr; const size_t off = (size_t)row * D + j0;
;                     const u32x4 yp = ypq[ai][mp][h]; float gsf[8];
;                     if (GATE_FP8) { v2u g8; g8.x = gq[h][0]; g8.y = gq[h][1]; const float k255 = 1.0f / 255.0f;
;                         gsf[0] = (float)(g8.x & 0xffu) * k255; gsf[1] = (float)((g8.x >> 8) & 0xffu) * k255; gsf[2] = (float)((g8.x >> 16) & 0xffu) * k255; gsf[3] = (float)(g8.x >> 24) * k255;
;                         gsf[4] = (float)(g8.y & 0xffu) * k255; gsf[5] = (float)((g8.y >> 8) & 0xffu) * k255; gsf[6] = (float)((g8.y >> 16) & 0xffu) * k255; gsf[7] = (float)(g8.y >> 24) * k255; }
;                     else { const u32x4 gs = *(const u32x4*)(SGS + off); gsf[0] = bf_lo(gs.x); gsf[1] = bf_hi(gs.x); gsf[2] = bf_lo(gs.y); gsf[3] = bf_hi(gs.y); gsf[4] = bf_lo(gs.z); gsf[5] = bf_hi(gs.z); gsf[6] = bf_lo(gs.w); gsf[7] = bf_hi(gs.w); }
;                     const f32x4 a0 = acc[ai][0][m][0] * asc + ba0, a1 = acc[ai][0][m][1] * asc + ba1, b0 = acc[ai][1][m][0] * asc + bb0, b1 = acc[ai][1][m][1] * asc + bb1;
;                     float o[8];
; #pragma unroll
;                     for (int j = 0; j < 4; ++j) { o[j] = a0[j] * sigmoidf_(b0[j]); o[4 + j] = a1[j] * sigmoidf_(b1[j]); }
;                     float mo[8] = {bf_lo(yp.x) + gsf[0] * o[0], bf_hi(yp.x) + gsf[1] * o[1], bf_lo(yp.y) + gsf[2] * o[2], bf_hi(yp.y) + gsf[3] * o[3],
;                                    bf_lo(yp.z) + gsf[4] * o[4], bf_hi(yp.z) + gsf[5] * o[5], bf_lo(yp.w) + gsf[6] * o[6], bf_hi(yp.w) + gsf[7] * o[7]};
;                     if (OUT_FP8) { px[h] = pk4_fp8(mo[0], mo[1], mo[2], mo[3]); py[h] = pk4_fp8(mo[4], mo[5], mo[6], mo[7]); }
;                     else { u32x4 w; w.x = cvt_pk_bf16(mo[0], mo[1]); w.y = cvt_pk_bf16(mo[2], mo[3]); w.z = cvt_pk_bf16(mo[4], mo[5]); w.w = cvt_pk_bf16(mo[6], mo[7]); *(u32x4*)(MG + off) = w; } }
;                 if (OUT_FP8) { const u32x4 q = pair16(px[0], py[0], px[1], py[1]);
	v_rcp_f32_e32 v54, v38
	v_add_f32_e32 v38, 1.0, v40
	v_fmamk_f32 v40, v111, 0x3d000000, v15
	v_cvt_pk_fp8_f32 v35, v36, v37 op_sel:[0,0,1]
	v_cvt_f32_ubyte0_e32 v37, v43
	v_cvt_f32_ubyte1_e32 v39, v43
	v_cvt_f32_ubyte2_e32 v41, v43
	v_cvt_f32_ubyte3_e32 v45, v43
	v_mul_f32_e32 v40, 0xbfb8aa3b, v40
	v_fmamk_f32 v43, v107, 0x3d000000, v11
	v_exp_f32_e32 v40, v40
	v_mul_f32_e32 v43, 0xbfb8aa3b, v43
	v_exp_f32_e32 v43, v43
	v_fmamk_f32 v44, v108, 0x3d000000, v12
	v_add_f32_e32 v40, 1.0, v40
	v_rcp_f32_e32 v62, v40
	v_add_f32_e32 v40, 1.0, v43
	v_fmamk_f32 v43, v112, 0x3d000000, v16
	v_mul_f32_e32 v43, 0xbfb8aa3b, v43
	v_exp_f32_e32 v43, v43
	v_mul_f32_e32 v44, 0xbfb8aa3b, v44
	v_exp_f32_e32 v44, v44
	v_fmamk_f32 v46, v98, 0x3d000000, v2
	v_add_f32_e32 v43, 1.0, v43
	v_rcp_f32_e32 v98, v43
	v_add_f32_e32 v43, 1.0, v44
	v_fmamk_f32 v50, v100, 0x3d000000, v4
	v_rcp_f32_e32 v100, v43
	v_fmamk_f32 v43, v113, 0x3d000000, v17
	v_mul_f32_e32 v43, 0xbfb8aa3b, v43
	v_fmamk_f32 v52, v109, 0x3d000000, v13
	v_exp_f32_e32 v43, v43
	v_mul_f32_e32 v52, 0xbfb8aa3b, v52
	v_exp_f32_e32 v55, v52
	v_rcp_f32_e32 v56, v38
	v_rcp_f32_e32 v64, v40
	v_add_f32_e32 v43, 1.0, v43
	v_fmamk_f32 v36, v102, 0x3d000000, v6
	v_rcp_f32_e32 v102, v43
	v_add_f32_e32 v43, 1.0, v55
	v_mov_b32_e32 v55, v212
	v_fmamk_f32 v38, v103, 0x3d000000, v7
	v_fmamk_f32 v48, v99, 0x3d000000, v3
	v_fmamk_f32 v40, v104, 0x3d000000, v8
	v_rcp_f32_e32 v104, v43
	v_pk_mul_f32 v[36:37], v[36:37], v[54:55]
	v_mov_b32_e32 v99, v212
	s_waitcnt vmcnt(5)
	v_lshlrev_b32_e32 v43, 16, v30
	v_cvt_f32_ubyte0_e32 v47, v61
	v_cvt_f32_ubyte1_e32 v49, v61
	v_pk_mul_f32 v[38:39], v[38:39], v[62:63]
	v_pk_mul_f32 v[40:41], v[40:41], v[98:99]
	v_fmac_f32_e32 v43, v36, v37
	v_and_b32_e32 v30, 0xffff0000, v30
	v_lshlrev_b32_e32 v36, 16, v31
	v_pk_mul_f32 v[46:47], v[46:47], v[56:57]
	v_pk_mul_f32 v[48:49], v[48:49], v[64:65]
	v_fmac_f32_e32 v30, v38, v39
	v_fmac_f32_e32 v36, v40, v41
	v_lshlrev_b32_e32 v37, 16, v32
	v_and_b32_e32 v32, 0xffff0000, v32
	v_fmac_f32_e32 v37, v46, v47
	v_fmac_f32_e32 v32, v48, v49
	v_med3_f32 v39, v43, s74, v227
	v_med3_f32 v30, v30, s74, v227
	v_med3_f32 v40, v36, s74, v227
	v_mov_b32_e32 v36, 0
	v_fmamk_f32 v44, v105, 0x3d000000, v9
	v_mov_b32_e32 v103, v212
	v_cvt_pk_fp8_f32 v36, v39, v30
	v_med3_f32 v30, v37, s74, v227
	v_med3_f32 v32, v32, s74, v227
	v_mov_b32_e32 v37, 0
	v_cvt_f32_ubyte2_e32 v51, v61
	v_cvt_f32_ubyte3_e32 v53, v61
	v_fmamk_f32 v52, v101, 0x3d000000, v5
	v_pk_mul_f32 v[44:45], v[44:45], v[102:103]
	v_mov_b32_e32 v101, v212
	v_mov_b32_e32 v105, v212
	v_and_b32_e32 v31, 0xffff0000, v31
	v_cvt_pk_fp8_f32 v37, v30, v32
	v_pk_mul_f32 v[50:51], v[50:51], v[100:101]
	v_pk_mul_f32 v[52:53], v[52:53], v[104:105]
	v_fmac_f32_e32 v31, v44, v45
	v_lshlrev_b32_e32 v38, 16, v33
	v_and_b32_e32 v33, 0xffff0000, v33
	v_fmac_f32_e32 v38, v50, v51
	v_fmac_f32_e32 v33, v52, v53
	v_med3_f32 v31, v31, s74, v227
	v_cvt_pk_fp8_f32 v36, v40, v31 op_sel:[0,0,1]
	v_med3_f32 v30, v38, s74, v227
	v_med3_f32 v31, v33, s74, v227
	v_add_u32_e32 v42, 0x80, v60
	v_cvt_pk_fp8_f32 v37, v30, v31 op_sel:[0,0,1]
	v_ashrrev_i32_e32 v43, 31, v42
	v_lshlrev_b64 v[30:31], 11, v[42:43]
	v_lshl_add_u64 v[30:31], s[16:17], 0, v[30:31]
	s_waitcnt vmcnt(4)
	v_mov_b32_e32 v61, v28
	v_permlane16_swap_b32_e32 v34, v36
	v_permlane16_swap_b32_e32 v35, v37
	v_lshl_add_u64 v[30:31], v[30:31], 0, v[58:59]
	v_permlane16_swap_b32_e32 v26, v61
	global_store_dwordx4 v[30:31], v[34:37], off
	v_mov_b32_e32 v62, v29
	v_cvt_f32_ubyte0_e32 v29, v26
	v_cvt_f32_ubyte1_e32 v31, v26
	v_cvt_f32_ubyte2_e32 v33, v26
	v_cvt_f32_ubyte3_e32 v35, v26
	v_fmamk_f32 v26, v94, 0x3d000000, v14
	v_mul_f32_e32 v26, 0xbfb8aa3b, v26
	v_fmamk_f32 v30, v90, 0x3d000000, v10
	v_exp_f32_e32 v26, v26
	v_mul_f32_e32 v30, 0xbfb8aa3b, v30
	v_exp_f32_e32 v30, v30
	v_fmamk_f32 v32, v91, 0x3d000000, v11
	v_add_f32_e32 v26, 1.0, v26
	v_rcp_f32_e32 v42, v26
	v_add_f32_e32 v26, 1.0, v30
	v_rcp_f32_e32 v44, v26
	v_fmamk_f32 v26, v95, 0x3d000000, v15
	v_mul_f32_e32 v26, 0xbfb8aa3b, v26
	v_exp_f32_e32 v26, v26
	v_mul_f32_e32 v32, 0xbfb8aa3b, v32
	v_exp_f32_e32 v32, v32
	v_fmamk_f32 v34, v92, 0x3d000000, v12
	v_add_f32_e32 v26, 1.0, v26
	v_rcp_f32_e32 v46, v26
	v_add_f32_e32 v26, 1.0, v32
	v_rcp_f32_e32 v48, v26
	v_fmamk_f32 v26, v96, 0x3d000000, v16
	v_mul_f32_e32 v26, 0xbfb8aa3b, v26
	v_exp_f32_e32 v26, v26
	v_mul_f32_e32 v34, 0xbfb8aa3b, v34
	v_exp_f32_e32 v34, v34
	v_fmamk_f32 v43, v93, 0x3d000000, v13
	v_add_f32_e32 v26, 1.0, v26
	v_rcp_f32_e32 v50, v26
	v_add_f32_e32 v26, 1.0, v34
	v_rcp_f32_e32 v52, v26
	v_fmamk_f32 v26, v97, 0x3d000000, v17
	v_mul_f32_e32 v26, 0xbfb8aa3b, v26
	v_mul_f32_e32 v43, 0xbfb8aa3b, v43
	v_exp_f32_e32 v26, v26
	v_exp_f32_e32 v43, v43
	v_fmamk_f32 v10, v74, 0x3d000000, v10
	v_mul_f32_e32 v10, 0xbfb8aa3b, v10
	v_add_f32_e32 v26, 1.0, v26
	v_add_f32_e32 v43, 1.0, v43
	v_rcp_f32_e32 v54, v26
	v_rcp_f32_e32 v56, v43
	v_permlane16_swap_b32_e32 v27, v62
	v_fmamk_f32 v28, v86, 0x3d000000, v6
	v_fmamk_f32 v30, v87, 0x3d000000, v7
	v_mov_b32_e32 v43, v212
	v_mov_b32_e32 v47, v212
	v_exp_f32_e32 v10, v10
	v_cvt_f32_ubyte0_e32 v37, v27
	v_cvt_f32_ubyte1_e32 v39, v27
	v_cvt_f32_ubyte2_e32 v41, v27
	v_cvt_f32_ubyte3_e32 v27, v27
	v_fmamk_f32 v36, v82, 0x3d000000, v2
	v_fmamk_f32 v38, v83, 0x3d000000, v3
	v_fmamk_f32 v34, v89, 0x3d000000, v9
	v_fmamk_f32 v26, v85, 0x3d000000, v5
	v_pk_mul_f32 v[28:29], v[28:29], v[42:43]
	v_pk_mul_f32 v[30:31], v[30:31], v[46:47]
	v_mov_b32_e32 v45, v212
	v_mov_b32_e32 v49, v212
	s_waitcnt vmcnt(4)
; #define PG8_BAR __builtin_amdgcn_s_barrier()
;     ...
;         if (wr == 0) PG8_BAR;
;     __device__ __forceinline__ void operator()(EPI_ARGS) const {
;     ...
;                 for (int h = 0; h < 2; ++h) { const int m = 2 * mp + h; const int row = u.pm * 256 + ai * 128 + wr * 64 + m * 16 + fr; const size_t off = (size_t)row * D + j0;
;                     const u32x4 yp = ypq[ai][mp][h]; float gsf[8];
;                     if (GATE_FP8) { v2u g8; g8.x = gq[h][0]; g8.y = gq[h][1]; const float k255 = 1.0f / 255.0f;
;                         gsf[0] = (float)(g8.x & 0xffu) * k255; gsf[1] = (float)((g8.x >> 8) & 0xffu) * k255; gsf[2] = (float)((g8.x >> 16) & 0xffu) * k255; gsf[3] = (float)(g8.x >> 24) * k255;
;                         gsf[4] = (float)(g8.y & 0xffu) * k255; gsf[5] = (float)((g8.y >> 8) & 0xffu) * k255; gsf[6] = (float)((g8.y >> 16) & 0xffu) * k255; gsf[7] = (float)(g8.y >> 24) * k255; }
;                     else { const u32x4 gs = *(const u32x4*)(SGS + off); gsf[0] = bf_lo(gs.x); gsf[1] = bf_hi(gs.x); gsf[2] = bf_lo(gs.y); gsf[3] = bf_hi(gs.y); gsf[4] = bf_lo(gs.z); gsf[5] = bf_hi(gs.z); gsf[6] = bf_lo(gs.w); gsf[7] = bf_hi(gs.w); }
;                     const f32x4 a0 = acc[ai][0][m][0] * asc + ba0, a1 = acc[ai][0][m][1] * asc + ba1, b0 = acc[ai][1][m][0] * asc + bb0, b1 = acc[ai][1][m][1] * asc + bb1;
;                     float o[8];
; #pragma unroll
;                     for (int j = 0; j < 4; ++j) { o[j] = a0[j] * sigmoidf_(b0[j]); o[4 + j] = a1[j] * sigmoidf_(b1[j]); }
;                     float mo[8] = {bf_lo(yp.x) + gsf[0] * o[0], bf_hi(yp.x) + gsf[1] * o[1], bf_lo(yp.y) + gsf[2] * o[2], bf_hi(yp.y) + gsf[3] * o[3],
;                                    bf_lo(yp.z) + gsf[4] * o[4], bf_hi(yp.z) + gsf[5] * o[5], bf_lo(yp.w) + gsf[6] * o[6], bf_hi(yp.w) + gsf[7] * o[7]};
;                     if (OUT_FP8) { px[h] = pk4_fp8(mo[0], mo[1], mo[2], mo[3]); py[h] = pk4_fp8(mo[4], mo[5], mo[6], mo[7]); }
;                     else { u32x4 w; w.x = cvt_pk_bf16(mo[0], mo[1]); w.y = cvt_pk_bf16(mo[2], mo[3]); w.z = cvt_pk_bf16(mo[4], mo[5]); w.w = cvt_pk_bf16(mo[6], mo[7]); *(u32x4*)(MG + off) = w; } }
;                 if (OUT_FP8) { const u32x4 q = pair16(px[0], py[0], px[1], py[1]);
;                     const int row = u.pm * 256 + ai * 128 + wr * 64 + (2 * mp + (fq & 1)) * 16 + fr; *(u32x4*)((unsigned char*)MG + (size_t)row * D + j0q) = q; } }
	v_lshlrev_b32_e32 v42, 16, v22
	v_and_b32_e32 v22, 0xffff0000, v22
	v_fmamk_f32 v32, v88, 0x3d000000, v8
	v_mov_b32_e32 v51, v212
	v_pk_mul_f32 v[34:35], v[34:35], v[54:55]
	v_pk_mul_f32 v[36:37], v[36:37], v[44:45]
	v_pk_mul_f32 v[38:39], v[38:39], v[48:49]
	v_pk_mul_f32 v[26:27], v[26:27], v[56:57]
	v_fmac_f32_e32 v42, v28, v29
	v_fmac_f32_e32 v22, v30, v31
	v_lshlrev_b32_e32 v28, 16, v23
	v_and_b32_e32 v23, 0xffff0000, v23
	v_lshlrev_b32_e32 v29, 16, v24
	v_and_b32_e32 v24, 0xffff0000, v24
	v_lshlrev_b32_e32 v30, 16, v25
	v_and_b32_e32 v25, 0xffff0000, v25
	v_pk_mul_f32 v[32:33], v[32:33], v[50:51]
	v_fmac_f32_e32 v23, v34, v35
	v_fmac_f32_e32 v29, v36, v37
	v_fmac_f32_e32 v24, v38, v39
	v_fmac_f32_e32 v25, v26, v27
	v_med3_f32 v26, v42, s74, v227
	v_med3_f32 v27, v22, s74, v227
	v_mov_b32_e32 v22, 0
	v_fmac_f32_e32 v28, v32, v33
	v_med3_f32 v31, v23, s74, v227
	v_cvt_pk_fp8_f32 v22, v26, v27
	v_med3_f32 v26, v29, s74, v227
	v_med3_f32 v24, v24, s74, v227
	v_mov_b32_e32 v23, 0
	v_fmamk_f32 v32, v66, 0x3d000000, v2
	v_add_f32_e32 v2, 1.0, v10
	v_fmamk_f32 v10, v75, 0x3d000000, v11
	v_cvt_pk_fp8_f32 v23, v26, v24
	v_fmamk_f32 v26, v71, 0x3d000000, v7
	v_fmamk_f32 v7, v79, 0x3d000000, v15
	v_mul_f32_e32 v10, 0xbfb8aa3b, v10
	v_mul_f32_e32 v7, 0xbfb8aa3b, v7
	v_exp_f32_e32 v11, v10
	v_fmamk_f32 v40, v84, 0x3d000000, v4
	v_mov_b32_e32 v53, v212
	v_exp_f32_e32 v7, v7
	v_pk_mul_f32 v[40:41], v[40:41], v[52:53]
	v_med3_f32 v25, v25, s74, v227
	v_fmac_f32_e32 v30, v40, v41
	v_med3_f32 v24, v30, s74, v227
	v_fmamk_f32 v34, v67, 0x3d000000, v3
	v_add_f32_e32 v3, 1.0, v11
	v_cvt_pk_fp8_f32 v23, v24, v25 op_sel:[0,0,1]
	v_fmamk_f32 v24, v70, 0x3d000000, v6
	v_fmamk_f32 v6, v78, 0x3d000000, v14
	v_add_f32_e32 v7, 1.0, v7
	v_rcp_f32_e32 v14, v3
	v_fmamk_f32 v3, v80, 0x3d000000, v16
	v_rcp_f32_e32 v10, v7
	v_mul_f32_e32 v3, 0xbfb8aa3b, v3
	v_fmamk_f32 v7, v76, 0x3d000000, v12
	v_exp_f32_e32 v3, v3
	v_mul_f32_e32 v7, 0xbfb8aa3b, v7
	v_exp_f32_e32 v7, v7
	v_mul_f32_e32 v6, 0xbfb8aa3b, v6
	v_exp_f32_e32 v6, v6
	v_add_f32_e32 v3, 1.0, v3
	v_med3_f32 v28, v28, s74, v227
	v_rcp_f32_e32 v12, v3
	v_add_f32_e32 v3, 1.0, v7
	v_fmac_f32_e32 v17, 0x3d000000, v81
	v_cvt_pk_fp8_f32 v22, v28, v31 op_sel:[0,0,1]
	v_fmamk_f32 v28, v72, 0x3d000000, v8
	v_rcp_f32_e32 v8, v3
	v_mul_f32_e32 v3, 0xbfb8aa3b, v17
	v_fmac_f32_e32 v13, 0x3d000000, v77
	v_fmamk_f32 v36, v68, 0x3d000000, v4
	v_exp_f32_e32 v3, v3
	v_mul_f32_e32 v4, 0xbfb8aa3b, v13
	v_add_f32_e32 v6, 1.0, v6
	v_exp_f32_e32 v4, v4
	v_rcp_f32_e32 v6, v6
	v_rcp_f32_e32 v2, v2
	v_add_f32_e32 v3, 1.0, v3
	v_cvt_f32_ubyte0_e32 v25, v61
	v_rcp_f32_e32 v16, v3
	v_add_f32_e32 v3, 1.0, v4
	v_mov_b32_e32 v7, v212
	v_cvt_f32_ubyte1_e32 v27, v61
	v_rcp_f32_e32 v4, v3
	v_pk_mul_f32 v[6:7], v[24:25], v[6:7]
	v_mov_b32_e32 v11, v212
	s_waitcnt vmcnt(3)
	v_lshlrev_b32_e32 v24, 16, v18
	v_cvt_f32_ubyte0_e32 v33, v62
	v_fmac_f32_e32 v9, 0x3d000000, v73
	v_pk_mul_f32 v[10:11], v[26:27], v[10:11]
	v_mov_b32_e32 v3, v212
	v_fmac_f32_e32 v24, v6, v7
	v_and_b32_e32 v6, 0xffff0000, v18
	v_cvt_f32_ubyte2_e32 v37, v62
	v_fmac_f32_e32 v5, 0x3d000000, v69
	v_mov_b32_e32 v30, v9
	v_pk_mul_f32 v[2:3], v[32:33], v[2:3]
	v_mov_b32_e32 v9, v212
	v_fmac_f32_e32 v6, v10, v11
	v_lshlrev_b32_e32 v11, 16, v20
	v_cvt_f32_ubyte1_e32 v35, v62
	v_cvt_f32_ubyte3_e32 v39, v62
	v_mov_b32_e32 v15, v212
	v_pk_mul_f32 v[8:9], v[36:37], v[8:9]
	v_mov_b32_e32 v38, v5
	v_mov_b32_e32 v5, v212
	v_fmac_f32_e32 v11, v2, v3
	v_lshlrev_b32_e32 v3, 16, v21
	v_pk_mul_f32 v[14:15], v[34:35], v[14:15]
	v_pk_mul_f32 v[4:5], v[38:39], v[4:5]
	v_and_b32_e32 v2, 0xffff0000, v20
	v_fmac_f32_e32 v3, v8, v9
	v_and_b32_e32 v8, 0xffff0000, v21
	v_fmac_f32_e32 v2, v14, v15
	v_fmac_f32_e32 v8, v4, v5
	v_med3_f32 v4, v24, s74, v227
	v_med3_f32 v5, v6, s74, v227
	v_mov_b32_e32 v24, 0
	v_cvt_pk_fp8_f32 v24, v4, v5
	v_med3_f32 v4, v11, s74, v227
	v_med3_f32 v2, v2, s74, v227
	v_mov_b32_e32 v25, 0
	v_cvt_f32_ubyte2_e32 v29, v61
	v_cvt_f32_ubyte3_e32 v31, v61
	v_mov_b32_e32 v13, v212
	v_mov_b32_e32 v17, v212
	v_cvt_pk_fp8_f32 v25, v4, v2
	v_pk_mul_f32 v[12:13], v[28:29], v[12:13]
	v_pk_mul_f32 v[16:17], v[30:31], v[16:17]
	v_lshlrev_b32_e32 v7, 16, v19
	v_and_b32_e32 v10, 0xffff0000, v19
	v_fmac_f32_e32 v7, v12, v13
	v_fmac_f32_e32 v10, v16, v17
	v_med3_f32 v6, v7, s74, v227
	v_med3_f32 v7, v10, s74, v227
	v_med3_f32 v2, v3, s74, v227
	v_med3_f32 v3, v8, s74, v227
	v_cvt_pk_fp8_f32 v24, v6, v7 op_sel:[0,0,1]
	v_cvt_pk_fp8_f32 v25, v2, v3 op_sel:[0,0,1]
	v_add_u32_e32 v2, 0xa0, v60
	v_ashrrev_i32_e32 v3, 31, v2
	v_lshlrev_b64 v[2:3], 11, v[2:3]
	v_lshl_add_u64 v[2:3], s[16:17], 0, v[2:3]
	v_permlane16_swap_b32_e32 v22, v24
	v_permlane16_swap_b32_e32 v23, v25
	v_lshl_add_u64 v[2:3], v[2:3], 0, v[58:59]
	s_mov_b64 s[4:5], -1
	global_store_dwordx4 v[2:3], v[22:25], off
	s_cbranch_vccnz .LBB0_885
	s_andn2_b64 vcc, exec, s[8:9]
	s_cbranch_vccnz .LBB0_884
	s_barrier
	s_branch .LBB0_884

; __device__ __forceinline__ unsigned cvt_pk_bf16(float lo, float hi) { unsigned r; asm volatile("v_cvt_pk_bf16_f32 %0, %1, %2" : "=v"(r) : "v"(lo), "v"(hi)); return r; }
; #define EPI_ALD16(dst_, ptr_) asm volatile("global_load_dwordx4 %0, %1, off" : "=v"(dst_) : "v"(ptr_))
;     ...
;         if constexpr (ESZ == 1) asm volatile("s_nop 15\n\ts_nop 15" ::: "memory");
;     __device__ __forceinline__ void operator()(EPI_ARGS) const {
;         const float* gb = gtm + (size_t)(u.pm >> 4) * 6 * D;
;         const float* xt = xin + (size_t)u.pm * 256 * D + u.pn * 256;
; #pragma unroll
;         for (int bj = 0; bj < 2; ++bj) { const int col = u.pn * 256 + bj * 128 + wc * 32 + 8 * fq; f32x4 g0, g1, xv[2][4][2];
;             EPI_ALD16(g0, gb + col); EPI_ALD16(g1, gb + col + 4);
; #pragma unroll
;             for (int ai = 0; ai < 2; ++ai)
; #pragma unroll
;                 for (int m = 0; m < 4; ++m) { const unsigned xo = (unsigned)((ai * 128 + wr * 64 + m * 16 + fr) * D + col - u.pn * 256) * 4u;
;                     asm volatile("global_load_dwordx4 %0, %1, %2" : "=v"(xv[ai][m][0]) : "v"(xo), "s"(xt)); asm volatile("global_load_dwordx4 %0, %1, %2 offset:16" : "=v"(xv[ai][m][1]) : "v"(xo), "s"(xt)); }
;             asm volatile("s_waitcnt vmcnt(0)" : "+v"(g0), "+v"(g1), "+v"(xv[0][0][0]), "+v"(xv[0][0][1]), "+v"(xv[0][1][0]), "+v"(xv[0][1][1]), "+v"(xv[0][2][0]), "+v"(xv[0][2][1]), "+v"(xv[0][3][0]), "+v"(xv[0][3][1]));
;             asm volatile("" : "+v"(xv[1][0][0]), "+v"(xv[1][0][1]), "+v"(xv[1][1][0]), "+v"(xv[1][1][1]), "+v"(xv[1][2][0]), "+v"(xv[1][2][1]), "+v"(xv[1][3][0]), "+v"(xv[1][3][1]));
;             g0 = g0 * asc; g1 = g1 * asc;
; #pragma unroll
;             for (int ai = 0; ai < 2; ++ai)
; #pragma unroll
;                 for (int m = 0; m < 4; ++m) { const int row = u.pm * 256 + ai * 128 + wr * 64 + m * 16 + fr; const f32x4 v0 = xv[ai][m][0] + acc[ai][bj][m][0] * g0, v1 = xv[ai][m][1] + acc[ai][bj][m][1] * g1;
;                     u32x4 w; w.x = cvt_pk_bf16(v0[0], v0[1]); w.y = cvt_pk_bf16(v0[2], v0[3]); w.z = cvt_pk_bf16(v1[0], v1[1]); w.w = cvt_pk_bf16(v1[2], v1[3]);
;                     *(u32x4*)(X1 + (size_t)row * D + col) = w; } }
.LBB0_995:
	s_ashr_i32 s14, s36, 4
	s_mul_i32 s14, s14, 6
	s_ashr_i32 s15, s14, 31
	s_lshl_b64 s[14:15], s[14:15], 13
	s_add_u32 s14, s63, s14
	s_addc_u32 s15, s64, s15
	s_ashr_i32 s37, s36, 31
	s_lshl_b64 s[38:39], s[36:37], 21
	s_add_u32 s25, s6, s38
	s_addc_u32 s27, s7, s39
	s_lshl_b32 s40, s72, 8
	s_ashr_i32 s41, s40, 31
	v_or_b32_e32 v244, s40, v195
	s_lshl_b64 s[38:39], s[40:41], 2
	v_ashrrev_i32_e32 v245, 31, v244
	s_add_u32 s38, s25, s38
	v_lshl_add_u64 v[18:19], v[244:245], 2, s[14:15]
	s_addc_u32 s39, s27, s39
	v_lshl_add_u64 v[2:3], v[18:19], 0, 16
	v_lshlrev_b32_e32 v246, 2, v244
	s_lshl_b32 s14, s72, 10
	s_nop 15
	s_nop 15
	global_load_dwordx4 v[20:23], v[18:19], off
	global_load_dwordx4 v[24:27], v[2:3], off
	v_subrev_u32_e32 v2, s14, v246
	v_add_u32_e32 v3, v2, v216
	global_load_dwordx4 v[30:33], v3, s[38:39]
	global_load_dwordx4 v[42:45], v3, s[38:39] offset:16
	v_add_u32_e32 v3, v2, v217
	global_load_dwordx4 v[46:49], v3, s[38:39]
	global_load_dwordx4 v[50:53], v3, s[38:39] offset:16
	v_add_u32_e32 v3, v2, v218
	global_load_dwordx4 v[54:57], v3, s[38:39]
	global_load_dwordx4 v[58:61], v3, s[38:39] offset:16
	v_add_u32_e32 v3, v2, v219
	global_load_dwordx4 v[62:65], v3, s[38:39]
	global_load_dwordx4 v[212:215], v3, s[38:39] offset:16
	v_add_u32_e32 v3, v2, v220
	global_load_dwordx4 v[228:231], v3, s[38:39]
	global_load_dwordx4 v[232:235], v3, s[38:39] offset:16
	v_add_u32_e32 v3, v2, v221
	global_load_dwordx4 v[236:239], v3, s[38:39]
	global_load_dwordx4 v[240:243], v3, s[38:39] offset:16
	v_add_u32_e32 v3, v2, v222
	v_add_u32_e32 v2, v2, v223
	v_lshl_add_u32 v28, s36, 8, v1
	global_load_dwordx4 v[14:17], v3, s[38:39]
	global_load_dwordx4 v[10:13], v3, s[38:39] offset:16
	global_load_dwordx4 v[6:9], v2, s[38:39]
	global_load_dwordx4 v[2:5], v2, s[38:39] offset:16
	v_ashrrev_i32_e32 v29, 31, v28
	s_waitcnt vmcnt(17)
	v_pk_mul_f32 v[38:39], v[22:23], s[20:21] op_sel_hi:[1,0]
	v_pk_mul_f32 v[40:41], v[20:21], s[20:21] op_sel_hi:[1,0]
	s_waitcnt vmcnt(15)
	v_pk_fma_f32 v[20:21], v[192:193], v[38:39], v[32:33]
	v_pk_fma_f32 v[22:23], v[190:191], v[40:41], v[30:31]
	v_pk_mul_f32 v[36:37], v[24:25], s[20:21] op_sel_hi:[1,0]
	v_cvt_pk_bf16_f32 v22, v22, v23
	v_cvt_pk_bf16_f32 v23, v20, v21
	v_lshlrev_b64 v[20:21], 12, v[28:29]
	s_waitcnt vmcnt(14)
	v_pk_fma_f32 v[24:25], v[186:187], v[36:37], v[42:43]
	v_lshl_add_u64 v[20:21], s[10:11], 0, v[20:21]
	v_lshlrev_b64 v[186:187], 1, v[244:245]
	v_pk_mul_f32 v[34:35], v[26:27], s[20:21] op_sel_hi:[1,0]
	v_lshl_add_u64 v[20:21], v[20:21], 0, v[186:187]
	v_pk_fma_f32 v[26:27], v[188:189], v[34:35], v[44:45]
	v_cvt_pk_bf16_f32 v24, v24, v25
	s_waitcnt vmcnt(12)
	v_pk_fma_f32 v[30:31], v[180:181], v[34:35], v[52:53]
	v_cvt_pk_bf16_f32 v25, v26, v27
	global_store_dwordx4 v[20:21], v[22:25], off
	v_pk_fma_f32 v[26:27], v[184:185], v[38:39], v[48:49]
	v_pk_fma_f32 v[32:33], v[178:179], v[36:37], v[50:51]
	v_or_b32_e32 v22, 16, v28
	v_ashrrev_i32_e32 v23, 31, v22
	v_lshlrev_b64 v[22:23], 12, v[22:23]
	v_pk_fma_f32 v[24:25], v[182:183], v[40:41], v[46:47]
	v_lshl_add_u64 v[22:23], s[10:11], 0, v[22:23]
	v_cvt_pk_bf16_f32 v24, v24, v25
	v_lshl_add_u64 v[22:23], v[22:23], 0, v[186:187]
	v_cvt_pk_bf16_f32 v25, v26, v27
	v_cvt_pk_bf16_f32 v26, v32, v33
	v_cvt_pk_bf16_f32 v27, v30, v31
	global_store_dwordx4 v[22:23], v[24:27], off
	s_waitcnt vmcnt(13)
	v_pk_fma_f32 v[30:31], v[174:175], v[40:41], v[54:55]
	s_waitcnt vmcnt(12)
	v_pk_fma_f32 v[32:33], v[170:171], v[36:37], v[58:59]
	v_or_b32_e32 v24, 32, v28
	v_pk_fma_f32 v[26:27], v[176:177], v[38:39], v[56:57]
	v_ashrrev_i32_e32 v25, 31, v24
	v_cvt_pk_bf16_f32 v30, v30, v31
	v_cvt_pk_bf16_f32 v31, v26, v27
	v_lshlrev_b64 v[24:25], 12, v[24:25]
	v_or_b32_e32 v26, 48, v28
	v_lshl_add_u64 v[24:25], s[10:11], 0, v[24:25]
	v_ashrrev_i32_e32 v27, 31, v26
	v_lshl_add_u64 v[24:25], v[24:25], 0, v[186:187]
	v_lshlrev_b64 v[26:27], 12, v[26:27]
	v_pk_fma_f32 v[42:43], v[172:173], v[34:35], v[60:61]
	v_cvt_pk_bf16_f32 v32, v32, v33
	v_lshl_add_u64 v[26:27], s[10:11], 0, v[26:27]
	v_cvt_pk_bf16_f32 v33, v42, v43
	global_store_dwordx4 v[24:25], v[30:33], off
	v_lshl_add_u64 v[26:27], v[26:27], 0, v[186:187]
	s_waitcnt vmcnt(11)
	v_pk_fma_f32 v[42:43], v[164:165], v[34:35], v[214:215]
	v_pk_fma_f32 v[30:31], v[166:167], v[40:41], v[62:63]
	v_pk_fma_f32 v[32:33], v[168:169], v[38:39], v[64:65]
	v_cvt_pk_bf16_f32 v30, v30, v31
	v_pk_fma_f32 v[44:45], v[162:163], v[36:37], v[212:213]
	v_cvt_pk_bf16_f32 v31, v32, v33
	s_waitcnt vmcnt(9)
	v_pk_fma_f32 v[46:47], v[156:157], v[34:35], v[234:235]
	v_cvt_pk_bf16_f32 v32, v44, v45
	v_cvt_pk_bf16_f32 v33, v42, v43
	global_store_dwordx4 v[26:27], v[30:33], off
	v_pk_fma_f32 v[42:43], v[158:159], v[40:41], v[228:229]
	v_pk_fma_f32 v[44:45], v[154:155], v[36:37], v[232:233]
	v_add_u32_e32 v30, 0x80, v28
	v_pk_fma_f32 v[32:33], v[160:161], v[38:39], v[230:231]
	v_ashrrev_i32_e32 v31, 31, v30
	v_cvt_pk_bf16_f32 v42, v42, v43
	v_cvt_pk_bf16_f32 v43, v32, v33
	v_lshlrev_b64 v[30:31], 12, v[30:31]
	v_add_u32_e32 v32, 0x90, v28
	v_lshl_add_u64 v[30:31], s[10:11], 0, v[30:31]
	v_ashrrev_i32_e32 v33, 31, v32
	v_lshl_add_u64 v[30:31], v[30:31], 0, v[186:187]
	v_lshlrev_b64 v[32:33], 12, v[32:33]
	v_cvt_pk_bf16_f32 v44, v44, v45
	v_cvt_pk_bf16_f32 v45, v46, v47
	global_store_dwordx4 v[30:31], v[42:45], off
	v_lshl_add_u64 v[32:33], s[10:11], 0, v[32:33]
	v_lshl_add_u64 v[32:33], v[32:33], 0, v[186:187]
	s_waitcnt vmcnt(10)
	v_pk_fma_f32 v[42:43], v[150:151], v[40:41], v[236:237]
	v_pk_fma_f32 v[44:45], v[152:153], v[38:39], v[238:239]
	v_cvt_pk_bf16_f32 v42, v42, v43
	s_waitcnt vmcnt(9)
; __device__ __forceinline__ unsigned cvt_pk_bf16(float lo, float hi) { unsigned r; asm volatile("v_cvt_pk_bf16_f32 %0, %1, %2" : "=v"(r) : "v"(lo), "v"(hi)); return r; }
;     ...
;         if (!has_next) break;
; #pragma unroll
;         for (int a = 0; a < 2; ++a)
; #pragma unroll
;             for (int b = 0; b < 2; ++b)
; #pragma unroll
;                 for (int m = 0; m < 4; ++m)
; #pragma unroll
;                     for (int n = 0; n < 2; ++n) acc[a][b][m][n] = (f32x4){0.f, 0.f, 0.f, 0.f};
;         cur = nxt; cA = nA; cB = nB; rotc = rotn; ++ui;
; #pragma unroll
;         for (int h = 0; h < 2; ++h)
; #pragma unroll
;             for (int i = 0; i < 2; ++i) gcur[h][i] = gnxt[h][i];
;         if (wr == 1) PG8_BAR;
;     __device__ __forceinline__ void operator()(EPI_ARGS) const {
;     ...
;         for (int bj = 0; bj < 2; ++bj) { const int col = u.pn * 256 + bj * 128 + wc * 32 + 8 * fq; f32x4 g0, g1, xv[2][4][2];
;             EPI_ALD16(g0, gb + col); EPI_ALD16(g1, gb + col + 4);
; #pragma unroll
;             for (int ai = 0; ai < 2; ++ai)
; #pragma unroll
;                 for (int m = 0; m < 4; ++m) { const unsigned xo = (unsigned)((ai * 128 + wr * 64 + m * 16 + fr) * D + col - u.pn * 256) * 4u;
;                     asm volatile("global_load_dwordx4 %0, %1, %2" : "=v"(xv[ai][m][0]) : "v"(xo), "s"(xt)); asm volatile("global_load_dwordx4 %0, %1, %2 offset:16" : "=v"(xv[ai][m][1]) : "v"(xo), "s"(xt)); }
;             asm volatile("s_waitcnt vmcnt(0)" : "+v"(g0), "+v"(g1), "+v"(xv[0][0][0]), "+v"(xv[0][0][1]), "+v"(xv[0][1][0]), "+v"(xv[0][1][1]), "+v"(xv[0][2][0]), "+v"(xv[0][2][1]), "+v"(xv[0][3][0]), "+v"(xv[0][3][1]));
;             asm volatile("" : "+v"(xv[1][0][0]), "+v"(xv[1][0][1]), "+v"(xv[1][1][0]), "+v"(xv[1][1][1]), "+v"(xv[1][2][0]), "+v"(xv[1][2][1]), "+v"(xv[1][3][0]), "+v"(xv[1][3][1]));
;             g0 = g0 * asc; g1 = g1 * asc;
; #pragma unroll
;             for (int ai = 0; ai < 2; ++ai)
; #pragma unroll
;                 for (int m = 0; m < 4; ++m) { const int row = u.pm * 256 + ai * 128 + wr * 64 + m * 16 + fr; const f32x4 v0 = xv[ai][m][0] + acc[ai][bj][m][0] * g0, v1 = xv[ai][m][1] + acc[ai][bj][m][1] * g1;
;                     u32x4 w; w.x = cvt_pk_bf16(v0[0], v0[1]); w.y = cvt_pk_bf16(v0[2], v0[3]); w.z = cvt_pk_bf16(v1[0], v1[1]); w.w = cvt_pk_bf16(v1[2], v1[3]);
;                     *(u32x4*)(X1 + (size_t)row * D + col) = w; } }
	v_pk_fma_f32 v[46:47], v[148:149], v[34:35], v[242:243]
	v_pk_fma_f32 v[48:49], v[146:147], v[36:37], v[240:241]
	v_cvt_pk_bf16_f32 v43, v44, v45
	s_waitcnt vmcnt(8)
	v_pk_fma_f32 v[14:15], v[142:143], v[40:41], v[14:15]
	v_cvt_pk_bf16_f32 v44, v48, v49
	v_cvt_pk_bf16_f32 v45, v46, v47
	global_store_dwordx4 v[32:33], v[42:45], off
	s_waitcnt vmcnt(8)
	v_pk_fma_f32 v[10:11], v[138:139], v[36:37], v[10:11]
	v_pk_fma_f32 v[16:17], v[144:145], v[38:39], v[16:17]
	v_add_u32_e32 v42, 0xa0, v28
	v_ashrrev_i32_e32 v43, 31, v42
	v_pk_fma_f32 v[44:45], v[140:141], v[34:35], v[12:13]
	v_cvt_pk_bf16_f32 v12, v14, v15
	v_cvt_pk_bf16_f32 v13, v16, v17
	v_cvt_pk_bf16_f32 v14, v10, v11
	v_lshlrev_b64 v[10:11], 12, v[42:43]
	v_lshl_add_u64 v[10:11], s[10:11], 0, v[10:11]
	v_lshl_add_u64 v[10:11], v[10:11], 0, v[186:187]
	v_cvt_pk_bf16_f32 v15, v44, v45
	global_store_dwordx4 v[10:11], v[12:15], off
	s_waitcnt vmcnt(8)
	v_pk_fma_f32 v[6:7], v[134:135], v[40:41], v[6:7]
	s_waitcnt vmcnt(7)
	v_pk_fma_f32 v[2:3], v[130:131], v[36:37], v[2:3]
	v_add_u32_e32 v12, 0xb0, v28
	v_ashrrev_i32_e32 v13, 31, v12
	v_pk_fma_f32 v[8:9], v[136:137], v[38:39], v[8:9]
	v_pk_fma_f32 v[14:15], v[132:133], v[34:35], v[4:5]
	v_cvt_pk_bf16_f32 v4, v6, v7
	v_cvt_pk_bf16_f32 v5, v8, v9
	v_cvt_pk_bf16_f32 v6, v2, v3
	v_lshlrev_b64 v[2:3], 12, v[12:13]
	v_lshl_add_u64 v[2:3], s[10:11], 0, v[2:3]
	v_lshl_add_u64 v[2:3], v[2:3], 0, v[186:187]
	v_cvt_pk_bf16_f32 v7, v14, v15
	global_store_dwordx4 v[2:3], v[4:7], off
	v_lshl_add_u64 v[8:9], v[18:19], 0, s[22:23]
	s_andn2_b64 vcc, exec, s[4:5]
	v_lshl_add_u64 v[4:5], v[18:19], 0, s[16:17]
	global_load_dwordx4 v[4:7], v[4:5], off
	global_load_dwordx4 v[12:15], v[8:9], off
	v_or_b32_e32 v8, 0x200, v246
	v_subrev_u32_e32 v8, s14, v8
	v_add_u32_e32 v9, v8, v216
	global_load_dwordx4 v[16:19], v9, s[38:39]
	global_load_dwordx4 v[34:37], v9, s[38:39] offset:16
	v_add_u32_e32 v9, v8, v217
	global_load_dwordx4 v[38:41], v9, s[38:39]
	global_load_dwordx4 v[42:45], v9, s[38:39] offset:16
	v_add_u32_e32 v9, v8, v218
	global_load_dwordx4 v[46:49], v9, s[38:39]
	global_load_dwordx4 v[50:53], v9, s[38:39] offset:16
	v_add_u32_e32 v9, v8, v219
	global_load_dwordx4 v[54:57], v9, s[38:39]
	global_load_dwordx4 v[58:61], v9, s[38:39] offset:16
	v_add_u32_e32 v9, v8, v220
	global_load_dwordx4 v[62:65], v9, s[38:39]
	global_load_dwordx4 v[130:133], v9, s[38:39] offset:16
	v_add_u32_e32 v9, v8, v221
	global_load_dwordx4 v[134:137], v9, s[38:39]
	global_load_dwordx4 v[138:141], v9, s[38:39] offset:16
	v_add_u32_e32 v9, v8, v222
	v_add_u32_e32 v8, v8, v223
	global_load_dwordx4 v[142:145], v9, s[38:39]
	global_load_dwordx4 v[146:149], v9, s[38:39] offset:16
	global_load_dwordx4 v[150:153], v8, s[38:39]
	global_load_dwordx4 v[154:157], v8, s[38:39] offset:16
	s_mov_b64 s[4:5], -1
	s_waitcnt vmcnt(17)
	v_pk_mul_f32 v[8:9], v[6:7], s[20:21] op_sel_hi:[1,0]
	v_pk_mul_f32 v[28:29], v[4:5], s[20:21] op_sel_hi:[1,0]
	s_waitcnt vmcnt(16)
	v_pk_mul_f32 v[14:15], v[14:15], s[20:21] op_sel_hi:[1,0]
	v_pk_mul_f32 v[12:13], v[12:13], s[20:21] op_sel_hi:[1,0]
	s_waitcnt vmcnt(15)
	v_pk_fma_f32 v[6:7], v[128:129], v[8:9], v[18:19]
	v_pk_fma_f32 v[4:5], v[126:127], v[28:29], v[16:17]
	s_waitcnt vmcnt(14)
	v_pk_fma_f32 v[16:17], v[124:125], v[14:15], v[36:37]
	v_pk_fma_f32 v[18:19], v[122:123], v[12:13], v[34:35]
	v_cvt_pk_bf16_f32 v4, v4, v5
	v_cvt_pk_bf16_f32 v5, v6, v7
	s_nop 0
	v_cvt_pk_bf16_f32 v6, v18, v19
	v_cvt_pk_bf16_f32 v7, v16, v17
	global_store_dwordx4 v[20:21], v[4:7], off offset:256
	s_waitcnt vmcnt(13)
	v_pk_fma_f32 v[16:17], v[116:117], v[14:15], v[44:45]
	v_pk_fma_f32 v[18:19], v[114:115], v[12:13], v[42:43]
	v_pk_fma_f32 v[6:7], v[120:121], v[8:9], v[40:41]
	v_pk_fma_f32 v[4:5], v[118:119], v[28:29], v[38:39]
	s_nop 0
	v_cvt_pk_bf16_f32 v4, v4, v5
	v_cvt_pk_bf16_f32 v5, v6, v7
	v_cvt_pk_bf16_f32 v6, v18, v19
	v_cvt_pk_bf16_f32 v7, v16, v17
	global_store_dwordx4 v[22:23], v[4:7], off offset:256
	s_waitcnt vmcnt(12)
	v_pk_fma_f32 v[16:17], v[100:101], v[14:15], v[52:53]
	v_pk_fma_f32 v[18:19], v[98:99], v[12:13], v[50:51]
	v_pk_fma_f32 v[6:7], v[112:113], v[8:9], v[48:49]
	v_pk_fma_f32 v[4:5], v[110:111], v[28:29], v[46:47]
	s_nop 0
	v_cvt_pk_bf16_f32 v4, v4, v5
	v_cvt_pk_bf16_f32 v5, v6, v7
	v_cvt_pk_bf16_f32 v6, v18, v19
	v_cvt_pk_bf16_f32 v7, v16, v17
	global_store_dwordx4 v[24:25], v[4:7], off offset:256
	s_waitcnt vmcnt(11)
	v_pk_fma_f32 v[16:17], v[84:85], v[14:15], v[60:61]
	v_pk_fma_f32 v[18:19], v[82:83], v[12:13], v[58:59]
	v_pk_fma_f32 v[6:7], v[88:89], v[8:9], v[56:57]
	v_pk_fma_f32 v[4:5], v[86:87], v[28:29], v[54:55]
	s_nop 0
	v_cvt_pk_bf16_f32 v4, v4, v5
	v_cvt_pk_bf16_f32 v5, v6, v7
	v_cvt_pk_bf16_f32 v6, v18, v19
	v_cvt_pk_bf16_f32 v7, v16, v17
	global_store_dwordx4 v[26:27], v[4:7], off offset:256
	s_waitcnt vmcnt(10)
	v_pk_fma_f32 v[16:17], v[104:105], v[14:15], v[132:133]
	v_pk_fma_f32 v[18:19], v[102:103], v[12:13], v[130:131]
	v_pk_fma_f32 v[6:7], v[108:109], v[8:9], v[64:65]
	v_pk_fma_f32 v[4:5], v[106:107], v[28:29], v[62:63]
	s_nop 0
	v_cvt_pk_bf16_f32 v4, v4, v5
	v_cvt_pk_bf16_f32 v5, v6, v7
	v_cvt_pk_bf16_f32 v6, v18, v19
	v_cvt_pk_bf16_f32 v7, v16, v17
	global_store_dwordx4 v[30:31], v[4:7], off offset:256
	s_waitcnt vmcnt(9)
	v_pk_fma_f32 v[16:17], v[92:93], v[14:15], v[140:141]
	v_pk_fma_f32 v[18:19], v[90:91], v[12:13], v[138:139]
	v_pk_fma_f32 v[6:7], v[96:97], v[8:9], v[136:137]
	v_pk_fma_f32 v[4:5], v[94:95], v[28:29], v[134:135]
	s_nop 0
	v_cvt_pk_bf16_f32 v4, v4, v5
	v_cvt_pk_bf16_f32 v5, v6, v7
	v_cvt_pk_bf16_f32 v6, v18, v19
	v_cvt_pk_bf16_f32 v7, v16, v17
	global_store_dwordx4 v[32:33], v[4:7], off offset:256
	s_waitcnt vmcnt(8)
	v_pk_fma_f32 v[16:17], v[76:77], v[14:15], v[148:149]
	v_pk_fma_f32 v[18:19], v[74:75], v[12:13], v[146:147]
	v_pk_fma_f32 v[6:7], v[80:81], v[8:9], v[144:145]
	v_pk_fma_f32 v[4:5], v[78:79], v[28:29], v[142:143]
	s_nop 0
	v_cvt_pk_bf16_f32 v4, v4, v5
	v_cvt_pk_bf16_f32 v5, v6, v7
	v_cvt_pk_bf16_f32 v6, v18, v19
	v_cvt_pk_bf16_f32 v7, v16, v17
	global_store_dwordx4 v[10:11], v[4:7], off offset:256
	s_waitcnt vmcnt(7)
	v_pk_fma_f32 v[10:11], v[66:67], v[12:13], v[154:155]
	s_nop 0
	v_pk_fma_f32 v[6:7], v[72:73], v[8:9], v[152:153]
	v_pk_fma_f32 v[4:5], v[70:71], v[28:29], v[150:151]
	v_pk_fma_f32 v[8:9], v[68:69], v[14:15], v[156:157]
	v_cvt_pk_bf16_f32 v4, v4, v5
	v_cvt_pk_bf16_f32 v5, v6, v7
	v_cvt_pk_bf16_f32 v6, v10, v11
	s_nop 0
	v_cvt_pk_bf16_f32 v7, v8, v9
	global_store_dwordx4 v[2:3], v[4:7], off offset:256
	s_cbranch_vccnz .LBB0_974
	s_andn2_b64 vcc, exec, s[8:9]
	s_cbranch_vccnz .LBB0_973
	s_barrier
	s_branch .LBB0_973
